# baseline (speedup 1.0000x reference)
.LBB3_35:
	s_andn2_b64 vcc, exec, s[2:3]
	s_cbranch_vccnz .LBB3_39
	s_waitcnt vmcnt(4)
	v_ashrrev_i32_e32 v81, 31, v80
	v_lshl_add_u64 v[2:3], v[80:81], 3, s[20:21]
	v_add_co_u32_e32 v2, vcc, 0x48000, v2
	s_movk_i32 s8, 0x620
	s_nop 0
	v_addc_co_u32_e32 v3, vcc, 0, v3, vcc
	global_load_dwordx2 v[82:83], v[2:3], off
	v_and_b32_e32 v2, 0x70, v7
	v_bitop3_b32 v2, v0, v2, 48 bitop3:0x6c
	s_waitcnt vmcnt(4)
	v_mad_u64_u32 v[64:65], s[6:7], v9, s8, v[2:3]
	v_lshrrev_b32_e32 v3, 4, v92
	v_bitop3_b32 v3, v3, v0, 4 bitop3:0x36
	v_lshlrev_b32_e32 v3, 4, v3
	v_and_b32_e32 v4, 0x70, v3
	s_waitcnt vmcnt(3)
	v_mad_u64_u32 v[66:67], s[6:7], v8, s8, v[4:5]
	s_waitcnt vmcnt(2)
	v_mad_u64_u32 v[68:69], s[6:7], v6, s8, v[2:3]
	s_waitcnt vmcnt(1)
	v_mad_u64_u32 v[70:71], s[6:7], v1, s8, v[4:5]
	v_lshrrev_b32_e32 v85, 5, v92
	v_bfe_u32 v2, v0, 1, 3
	s_mov_b64 s[6:7], 0x1800
	s_add_u32 s4, s20, 0x4000000
	v_bitop3_b32 v32, v85, v2, 2 bitop3:0x36
	v_bitop3_b32 v33, v85, v2, 4 bitop3:0x36
	v_bitop3_b32 v34, v85, v2, 6 bitop3:0x36
	v_lshl_add_u64 v[2:3], v[86:87], 0, s[6:7]
	s_addc_u32 s5, s21, 0
	s_lshl_b32 s2, s27, 12
	s_addk_i32 s2, 0x6000
	v_lshrrev_b32_e32 v1, 1, v0
	v_or_b32_e32 v81, s2, v84
	v_lshlrev_b32_e32 v0, 7, v0
	v_and_b32_e32 v8, 0xf80, v0
	v_lshlrev_b32_e32 v9, 4, v32
	v_bitop3_b32 v1, v85, v1, 7 bitop3:0x78
	v_or3_b32 v96, s2, v9, v8
	v_lshlrev_b32_e32 v9, 4, v33
	v_lshlrev_b32_e32 v1, 4, v1
	v_or3_b32 v97, s2, v9, v8
	v_lshlrev_b32_e32 v9, 4, v34
	v_or3_b32 v95, s2, v1, v8
	v_or3_b32 v94, s2, v9, v8
	v_add_u32_e32 v98, 0x103c0, v84
	global_load_dwordx4 v[116:119], v64, s[4:5] offset:0
	global_load_dwordx4 v[120:123], v66, s[4:5] offset:0
	global_load_dwordx4 v[124:127], v68, s[4:5] offset:0
	global_load_dwordx4 v[128:131], v70, s[4:5] offset:0
	global_load_dwordx4 v[132:135], v64, s[4:5] offset:128
	global_load_dwordx4 v[136:139], v66, s[4:5] offset:128
	global_load_dwordx4 v[140:143], v68, s[4:5] offset:128
	global_load_dwordx4 v[144:147], v70, s[4:5] offset:128
	global_load_dwordx4 v[148:151], v64, s[4:5] offset:256
	global_load_dwordx4 v[152:155], v66, s[4:5] offset:256
	global_load_dwordx4 v[156:159], v68, s[4:5] offset:256
	global_load_dwordx4 v[72:75], v70, s[4:5] offset:256
	s_add_u32 m0, s46, 0x0
	s_nop 0
	global_load_lds_dwordx4 v76, s[40:41]
	s_add_u32 m0, s47, 0x0
	s_nop 0
	global_load_lds_dwordx4 v77, s[42:43]
	s_add_u32 m0, s48, 0x0
	s_nop 0
	global_load_lds_dwordx4 v78, s[44:45]
	s_add_u32 m0, s46, 0x3000
	s_add_u32 s40, s40, 0x1800
	s_addc_u32 s41, s41, 0
	global_load_lds_dwordx4 v76, s[40:41]
	s_add_u32 m0, s47, 0x3000
	s_add_u32 s42, s42, 0x1800
	s_addc_u32 s43, s43, 0
	global_load_lds_dwordx4 v77, s[42:43]
	s_add_u32 m0, s48, 0x3000
	s_add_u32 s44, s44, 0x1800
	s_addc_u32 s45, s45, 0
	global_load_lds_dwordx4 v78, s[44:45]
	s_add_u32 m0, s46, 0xd3c0
	s_add_u32 s40, s40, 0x1800
	s_addc_u32 s41, s41, 0
	global_load_lds_dwordx4 v76, s[40:41]
	s_add_u32 m0, s47, 0xd3c0
	s_add_u32 s42, s42, 0x1800
	s_addc_u32 s43, s43, 0
	global_load_lds_dwordx4 v77, s[42:43]
	s_add_u32 m0, s48, 0xd3c0
	s_add_u32 s44, s44, 0x1800
	s_addc_u32 s45, s45, 0
	global_load_lds_dwordx4 v78, s[44:45]
	s_add_u32 m0, s46, 0x103c0
	s_add_u32 s40, s40, 0x1800
	s_addc_u32 s41, s41, 0
	global_load_lds_dwordx4 v76, s[40:41]
	s_add_u32 m0, s47, 0x103c0
	s_add_u32 s42, s42, 0x1800
	s_addc_u32 s43, s43, 0
	global_load_lds_dwordx4 v77, s[42:43]
	s_add_u32 m0, s48, 0x103c0
	s_add_u32 s44, s44, 0x1800
	s_addc_u32 s45, s45, 0
	global_load_lds_dwordx4 v78, s[44:45]
	s_waitcnt vmcnt(20)
	ds_write_b128 v81, v[116:119]
	ds_write_b128 v81, v[120:123] offset:1024
	ds_write_b128 v81, v[124:127] offset:2048
	ds_write_b128 v81, v[128:131] offset:3072
	ds_read_b128 v[52:55], v95
	ds_read_b128 v[56:59], v96
	ds_read_b128 v[60:63], v97
	ds_read_b128 v[0:3], v94
	global_load_dwordx4 v[116:119], v64, s[4:5] offset:384
	global_load_dwordx4 v[120:123], v66, s[4:5] offset:384
	global_load_dwordx4 v[124:127], v68, s[4:5] offset:384
	global_load_dwordx4 v[128:131], v70, s[4:5] offset:384
	s_waitcnt vmcnt(13)
	s_waitcnt lgkmcnt(0)
	s_barrier
	ds_read_b128 v[4:7], v84 offset:0
	ds_read_b128 v[8:11], v84 offset:1024
	ds_read_b128 v[12:15], v84 offset:2048
	ds_read_b128 v[16:19], v84 offset:3072
	ds_read_b128 v[20:23], v84 offset:4096
	ds_read_b128 v[24:27], v84 offset:5120
	ds_read_b128 v[28:31], v84 offset:6144
	ds_read_b128 v[32:35], v84 offset:7168
	ds_read_b128 v[36:39], v84 offset:8192
	ds_read_b128 v[40:43], v84 offset:9216
	ds_read_b128 v[44:47], v84 offset:10240
	ds_read_b128 v[48:51], v84 offset:11264
	s_waitcnt lgkmcnt(6)
	v_mfma_f32_32x32x16_f16 a[80:95], v[4:7], v[52:55], 0
	v_mfma_f32_32x32x16_f16 a[64:79], v[8:11], v[52:55], 0
	v_mfma_f32_32x32x16_f16 a[48:63], v[12:15], v[52:55], 0
	v_mfma_f32_32x32x16_f16 a[32:47], v[16:19], v[52:55], 0
	s_waitcnt vmcnt(10)
	s_waitcnt lgkmcnt(0)
	s_barrier
	ds_read_b128 v[4:7], v84 offset:12288
	ds_read_b128 v[8:11], v84 offset:13312
	ds_read_b128 v[12:15], v84 offset:14336
	ds_read_b128 v[16:19], v84 offset:15360
	v_mfma_f32_32x32x16_f16 a[16:31], v[20:23], v[52:55], 0
	ds_read_b128 v[20:23], v84 offset:16384
	v_mfma_f32_32x32x16_f16 a[0:15], v[24:27], v[52:55], 0
	ds_read_b128 v[24:27], v84 offset:17408
	v_mfma_f32_32x32x16_f16 a[80:95], v[28:31], v[56:59], a[80:95]
	s_add_u32 m0, s46, 0x0
	s_add_u32 s40, s40, 0x1800
	s_addc_u32 s41, s41, 0
	global_load_lds_dwordx4 v76, s[40:41]
	ds_read_b128 v[28:31], v84 offset:18432
	v_mfma_f32_32x32x16_f16 a[64:79], v[32:35], v[56:59], a[64:79]
	ds_read_b128 v[32:35], v84 offset:19456
	v_mfma_f32_32x32x16_f16 a[48:63], v[36:39], v[56:59], a[48:63]
	s_add_u32 m0, s47, 0x0
	s_add_u32 s42, s42, 0x1800
	s_addc_u32 s43, s43, 0
	global_load_lds_dwordx4 v77, s[42:43]
	ds_read_b128 v[36:39], v84 offset:20480
	v_mfma_f32_32x32x16_f16 a[32:47], v[40:43], v[56:59], a[32:47]
	ds_read_b128 v[40:43], v84 offset:21504
	v_mfma_f32_32x32x16_f16 a[16:31], v[44:47], v[56:59], a[16:31]
	s_add_u32 m0, s48, 0x0
	s_add_u32 s44, s44, 0x1800
	s_addc_u32 s45, s45, 0
	global_load_lds_dwordx4 v78, s[44:45]
	ds_read_b128 v[44:47], v84 offset:22528
	v_mfma_f32_32x32x16_f16 a[0:15], v[48:51], v[56:59], a[0:15]
	ds_read_b128 v[48:51], v84 offset:23552
	s_waitcnt lgkmcnt(6)
	v_mfma_f32_32x32x16_f16 a[80:95], v[4:7], v[60:63], a[80:95]
	s_waitcnt vmcnt(23)
	ds_write_b128 v81, v[132:135]
	ds_write_b128 v81, v[136:139] offset:1024
	v_mfma_f32_32x32x16_f16 a[64:79], v[8:11], v[60:63], a[64:79]
	ds_write_b128 v81, v[140:143] offset:2048
	ds_write_b128 v81, v[144:147] offset:3072
	v_mfma_f32_32x32x16_f16 a[48:63], v[12:15], v[60:63], a[48:63]
	ds_read_b128 v[100:103], v95
	ds_read_b128 v[104:107], v96
	ds_read_b128 v[108:111], v97
	ds_read_b128 v[112:115], v94
	v_mfma_f32_32x32x16_f16 a[32:47], v[16:19], v[60:63], a[32:47]
	s_waitcnt vmcnt(10)
	s_waitcnt lgkmcnt(8)
	s_barrier
	ds_read_b128 v[4:7], v84 offset:54208
	ds_read_b128 v[8:11], v84 offset:55232
	ds_read_b128 v[12:15], v84 offset:56256
	ds_read_b128 v[16:19], v84 offset:57280
	v_mfma_f32_32x32x16_f16 a[16:31], v[20:23], v[60:63], a[16:31]
	ds_read_b128 v[20:23], v84 offset:58304
	v_mfma_f32_32x32x16_f16 a[0:15], v[24:27], v[60:63], a[0:15]
	ds_read_b128 v[24:27], v84 offset:59328
	s_waitcnt lgkmcnt(6)
	v_mfma_f32_32x32x16_f16 a[80:95], v[28:31], v[0:3], a[80:95]
	s_add_u32 m0, s46, 0x3000
	s_add_u32 s40, s40, 0x1800
	s_addc_u32 s41, s41, 0
	global_load_lds_dwordx4 v76, s[40:41]
	ds_read_b128 v[28:31], v84 offset:60352
	v_mfma_f32_32x32x16_f16 a[64:79], v[32:35], v[0:3], a[64:79]
	global_load_dwordx4 v[132:135], v64, s[4:5] offset:512
	global_load_dwordx4 v[136:139], v66, s[4:5] offset:512
	ds_read_b128 v[32:35], v84 offset:61376
	v_mfma_f32_32x32x16_f16 a[48:63], v[36:39], v[0:3], a[48:63]
	s_add_u32 m0, s47, 0x3000
	s_add_u32 s42, s42, 0x1800
	s_addc_u32 s43, s43, 0
	global_load_lds_dwordx4 v77, s[42:43]
	ds_read_b128 v[36:39], v84 offset:62400
	v_mfma_f32_32x32x16_f16 a[32:47], v[40:43], v[0:3], a[32:47]
	global_load_dwordx4 v[140:143], v68, s[4:5] offset:512
	global_load_dwordx4 v[144:147], v70, s[4:5] offset:512
	ds_read_b128 v[40:43], v84 offset:63424
	v_mfma_f32_32x32x16_f16 a[16:31], v[44:47], v[0:3], a[16:31]
	s_add_u32 m0, s48, 0x3000
	s_add_u32 s44, s44, 0x1800
	s_addc_u32 s45, s45, 0
	global_load_lds_dwordx4 v78, s[44:45]
	ds_read_b128 v[44:47], v84 offset:64448
	v_mfma_f32_32x32x16_f16 a[0:15], v[48:51], v[0:3], a[0:15]
	ds_read_b128 v[48:51], v84 offset:65472
	s_waitcnt lgkmcnt(6)
	v_mfma_f32_32x32x16_f16 a[80:95], v[4:7], v[100:103], a[80:95]
	v_mfma_f32_32x32x16_f16 a[64:79], v[8:11], v[100:103], a[64:79]
	v_mfma_f32_32x32x16_f16 a[48:63], v[12:15], v[100:103], a[48:63]
	v_mfma_f32_32x32x16_f16 a[32:47], v[16:19], v[100:103], a[32:47]
	s_waitcnt vmcnt(14)
	s_waitcnt lgkmcnt(0)
	s_barrier
	ds_read_b128 v[4:7], v98
	ds_read_b128 v[8:11], v98 offset:1024
	ds_read_b128 v[12:15], v98 offset:2048
	ds_read_b128 v[16:19], v98 offset:3072
	v_mfma_f32_32x32x16_f16 a[16:31], v[20:23], v[100:103], a[16:31]
	ds_read_b128 v[20:23], v98 offset:4096
	v_mfma_f32_32x32x16_f16 a[0:15], v[24:27], v[100:103], a[0:15]
	ds_read_b128 v[24:27], v98 offset:5120
	v_mfma_f32_32x32x16_f16 a[80:95], v[28:31], v[104:107], a[80:95]
	s_add_u32 m0, s46, 0xd3c0
	s_add_u32 s40, s40, 0x1800
	s_addc_u32 s41, s41, 0
	global_load_lds_dwordx4 v76, s[40:41]
	ds_read_b128 v[28:31], v98 offset:6144
	v_mfma_f32_32x32x16_f16 a[64:79], v[32:35], v[104:107], a[64:79]
	ds_read_b128 v[32:35], v98 offset:7168
	v_mfma_f32_32x32x16_f16 a[48:63], v[36:39], v[104:107], a[48:63]
	s_add_u32 m0, s47, 0xd3c0
	s_add_u32 s42, s42, 0x1800
	s_addc_u32 s43, s43, 0
	global_load_lds_dwordx4 v77, s[42:43]
	ds_read_b128 v[36:39], v98 offset:8192
	v_mfma_f32_32x32x16_f16 a[32:47], v[40:43], v[104:107], a[32:47]
	ds_read_b128 v[40:43], v98 offset:9216
	v_mfma_f32_32x32x16_f16 a[16:31], v[44:47], v[104:107], a[16:31]
	s_add_u32 m0, s48, 0xd3c0
	s_add_u32 s44, s44, 0x1800
	s_addc_u32 s45, s45, 0
	global_load_lds_dwordx4 v78, s[44:45]
	ds_read_b128 v[44:47], v98 offset:10240
	v_mfma_f32_32x32x16_f16 a[0:15], v[48:51], v[104:107], a[0:15]
	ds_read_b128 v[48:51], v98 offset:11264
	s_waitcnt lgkmcnt(6)
	v_mfma_f32_32x32x16_f16 a[80:95], v[4:7], v[108:111], a[80:95]
	s_waitcnt vmcnt(29)
	ds_write_b128 v81, v[148:151]
	ds_write_b128 v81, v[152:155] offset:1024
	v_mfma_f32_32x32x16_f16 a[64:79], v[8:11], v[108:111], a[64:79]
	ds_write_b128 v81, v[156:159] offset:2048
	ds_write_b128 v81, v[72:75] offset:3072
	v_mfma_f32_32x32x16_f16 a[48:63], v[12:15], v[108:111], a[48:63]
	ds_read_b128 v[52:55], v95
	ds_read_b128 v[56:59], v96
	ds_read_b128 v[60:63], v97
	ds_read_b128 v[0:3], v94
	v_mfma_f32_32x32x16_f16 a[32:47], v[16:19], v[108:111], a[32:47]
	s_waitcnt vmcnt(10)
	s_waitcnt lgkmcnt(8)
	s_barrier
	ds_read_b128 v[4:7], v84 offset:0
	ds_read_b128 v[8:11], v84 offset:1024
	ds_read_b128 v[12:15], v84 offset:2048
	ds_read_b128 v[16:19], v84 offset:3072
	v_mfma_f32_32x32x16_f16 a[16:31], v[20:23], v[108:111], a[16:31]
	ds_read_b128 v[20:23], v84 offset:4096
	v_mfma_f32_32x32x16_f16 a[0:15], v[24:27], v[108:111], a[0:15]
	ds_read_b128 v[24:27], v84 offset:5120
	s_waitcnt lgkmcnt(6)
	v_mfma_f32_32x32x16_f16 a[80:95], v[28:31], v[112:115], a[80:95]
	s_add_u32 m0, s46, 0x103c0
	s_add_u32 s40, s40, 0x1800
	s_addc_u32 s41, s41, 0
	global_load_lds_dwordx4 v76, s[40:41]
	ds_read_b128 v[28:31], v84 offset:6144
	v_mfma_f32_32x32x16_f16 a[64:79], v[32:35], v[112:115], a[64:79]
	global_load_dwordx4 v[148:151], v64, s[4:5] offset:640
	global_load_dwordx4 v[152:155], v66, s[4:5] offset:640
	ds_read_b128 v[32:35], v84 offset:7168
	v_mfma_f32_32x32x16_f16 a[48:63], v[36:39], v[112:115], a[48:63]
	s_add_u32 m0, s47, 0x103c0
	s_add_u32 s42, s42, 0x1800
	s_addc_u32 s43, s43, 0
	global_load_lds_dwordx4 v77, s[42:43]
	ds_read_b128 v[36:39], v84 offset:8192
	v_mfma_f32_32x32x16_f16 a[32:47], v[40:43], v[112:115], a[32:47]
	global_load_dwordx4 v[156:159], v68, s[4:5] offset:640
	global_load_dwordx4 v[72:75], v70, s[4:5] offset:640
	ds_read_b128 v[40:43], v84 offset:9216
	v_mfma_f32_32x32x16_f16 a[16:31], v[44:47], v[112:115], a[16:31]
	s_add_u32 m0, s48, 0x103c0
	s_add_u32 s44, s44, 0x1800
	s_addc_u32 s45, s45, 0
	global_load_lds_dwordx4 v78, s[44:45]
	ds_read_b128 v[44:47], v84 offset:10240
	v_mfma_f32_32x32x16_f16 a[0:15], v[48:51], v[112:115], a[0:15]
	ds_read_b128 v[48:51], v84 offset:11264
	s_waitcnt lgkmcnt(6)
	v_mfma_f32_32x32x16_f16 a[80:95], v[4:7], v[52:55], a[80:95]
	v_mfma_f32_32x32x16_f16 a[64:79], v[8:11], v[52:55], a[64:79]
	v_mfma_f32_32x32x16_f16 a[48:63], v[12:15], v[52:55], a[48:63]
	v_mfma_f32_32x32x16_f16 a[32:47], v[16:19], v[52:55], a[32:47]
	s_waitcnt vmcnt(10)
	s_waitcnt lgkmcnt(0)
	s_barrier
	ds_read_b128 v[4:7], v84 offset:12288
	ds_read_b128 v[8:11], v84 offset:13312
	ds_read_b128 v[12:15], v84 offset:14336
	ds_read_b128 v[16:19], v84 offset:15360
	v_mfma_f32_32x32x16_f16 a[16:31], v[20:23], v[52:55], a[16:31]
	ds_read_b128 v[20:23], v84 offset:16384
	v_mfma_f32_32x32x16_f16 a[0:15], v[24:27], v[52:55], a[0:15]
	ds_read_b128 v[24:27], v84 offset:17408
	v_mfma_f32_32x32x16_f16 a[80:95], v[28:31], v[56:59], a[80:95]
	s_add_u32 m0, s46, 0x0
	s_add_u32 s40, s40, 0x1800
	s_addc_u32 s41, s41, 0
	global_load_lds_dwordx4 v76, s[40:41]
	ds_read_b128 v[28:31], v84 offset:18432
	v_mfma_f32_32x32x16_f16 a[64:79], v[32:35], v[56:59], a[64:79]
	ds_read_b128 v[32:35], v84 offset:19456
	v_mfma_f32_32x32x16_f16 a[48:63], v[36:39], v[56:59], a[48:63]
	s_add_u32 m0, s47, 0x0
	s_add_u32 s42, s42, 0x1800
	s_addc_u32 s43, s43, 0
	global_load_lds_dwordx4 v77, s[42:43]
	ds_read_b128 v[36:39], v84 offset:20480
	v_mfma_f32_32x32x16_f16 a[32:47], v[40:43], v[56:59], a[32:47]
	ds_read_b128 v[40:43], v84 offset:21504
	v_mfma_f32_32x32x16_f16 a[16:31], v[44:47], v[56:59], a[16:31]
	s_add_u32 m0, s48, 0x0
	s_add_u32 s44, s44, 0x1800
	s_addc_u32 s45, s45, 0
	global_load_lds_dwordx4 v78, s[44:45]
	ds_read_b128 v[44:47], v84 offset:22528
	v_mfma_f32_32x32x16_f16 a[0:15], v[48:51], v[56:59], a[0:15]
	ds_read_b128 v[48:51], v84 offset:23552
	s_waitcnt lgkmcnt(6)
	v_mfma_f32_32x32x16_f16 a[80:95], v[4:7], v[60:63], a[80:95]
	s_waitcnt vmcnt(23)
	ds_write_b128 v81, v[116:119]
	ds_write_b128 v81, v[120:123] offset:1024
	v_mfma_f32_32x32x16_f16 a[64:79], v[8:11], v[60:63], a[64:79]
	ds_write_b128 v81, v[124:127] offset:2048
	ds_write_b128 v81, v[128:131] offset:3072
	v_mfma_f32_32x32x16_f16 a[48:63], v[12:15], v[60:63], a[48:63]
	ds_read_b128 v[100:103], v95
	ds_read_b128 v[104:107], v96
	ds_read_b128 v[108:111], v97
	ds_read_b128 v[112:115], v94
	v_mfma_f32_32x32x16_f16 a[32:47], v[16:19], v[60:63], a[32:47]
	s_waitcnt vmcnt(10)
	s_waitcnt lgkmcnt(8)
	s_barrier
	ds_read_b128 v[4:7], v84 offset:54208
	ds_read_b128 v[8:11], v84 offset:55232
	ds_read_b128 v[12:15], v84 offset:56256
	ds_read_b128 v[16:19], v84 offset:57280
	v_mfma_f32_32x32x16_f16 a[16:31], v[20:23], v[60:63], a[16:31]
	ds_read_b128 v[20:23], v84 offset:58304
	v_mfma_f32_32x32x16_f16 a[0:15], v[24:27], v[60:63], a[0:15]
	ds_read_b128 v[24:27], v84 offset:59328
	s_waitcnt lgkmcnt(6)
	v_mfma_f32_32x32x16_f16 a[80:95], v[28:31], v[0:3], a[80:95]
	s_add_u32 m0, s46, 0x3000
	s_add_u32 s40, s40, 0x1800
	s_addc_u32 s41, s41, 0
	global_load_lds_dwordx4 v76, s[40:41]
	ds_read_b128 v[28:31], v84 offset:60352
	v_mfma_f32_32x32x16_f16 a[64:79], v[32:35], v[0:3], a[64:79]
	global_load_dwordx4 v[116:119], v64, s[4:5] offset:768
	global_load_dwordx4 v[120:123], v66, s[4:5] offset:768
	ds_read_b128 v[32:35], v84 offset:61376
	v_mfma_f32_32x32x16_f16 a[48:63], v[36:39], v[0:3], a[48:63]
	s_add_u32 m0, s47, 0x3000
	s_add_u32 s42, s42, 0x1800
	s_addc_u32 s43, s43, 0
	global_load_lds_dwordx4 v77, s[42:43]
	ds_read_b128 v[36:39], v84 offset:62400
	v_mfma_f32_32x32x16_f16 a[32:47], v[40:43], v[0:3], a[32:47]
	global_load_dwordx4 v[124:127], v68, s[4:5] offset:768
	global_load_dwordx4 v[128:131], v70, s[4:5] offset:768
	ds_read_b128 v[40:43], v84 offset:63424
	v_mfma_f32_32x32x16_f16 a[16:31], v[44:47], v[0:3], a[16:31]
	s_add_u32 m0, s48, 0x3000
	s_add_u32 s44, s44, 0x1800
	s_addc_u32 s45, s45, 0
	global_load_lds_dwordx4 v78, s[44:45]
	ds_read_b128 v[44:47], v84 offset:64448
	v_mfma_f32_32x32x16_f16 a[0:15], v[48:51], v[0:3], a[0:15]
	ds_read_b128 v[48:51], v84 offset:65472
	s_waitcnt lgkmcnt(6)
	v_mfma_f32_32x32x16_f16 a[80:95], v[4:7], v[100:103], a[80:95]
	v_mfma_f32_32x32x16_f16 a[64:79], v[8:11], v[100:103], a[64:79]
	v_mfma_f32_32x32x16_f16 a[48:63], v[12:15], v[100:103], a[48:63]
	v_mfma_f32_32x32x16_f16 a[32:47], v[16:19], v[100:103], a[32:47]
	s_waitcnt vmcnt(10)
	s_waitcnt lgkmcnt(0)
	s_barrier
	ds_read_b128 v[4:7], v98
	ds_read_b128 v[8:11], v98 offset:1024
	ds_read_b128 v[12:15], v98 offset:2048
	ds_read_b128 v[16:19], v98 offset:3072
	v_mfma_f32_32x32x16_f16 a[16:31], v[20:23], v[100:103], a[16:31]
	ds_read_b128 v[20:23], v98 offset:4096
	v_mfma_f32_32x32x16_f16 a[0:15], v[24:27], v[100:103], a[0:15]
	ds_read_b128 v[24:27], v98 offset:5120
	v_mfma_f32_32x32x16_f16 a[80:95], v[28:31], v[104:107], a[80:95]
	s_add_u32 m0, s46, 0xd3c0
	s_add_u32 s40, s40, 0x1800
	s_addc_u32 s41, s41, 0
	global_load_lds_dwordx4 v76, s[40:41]
	ds_read_b128 v[28:31], v98 offset:6144
	v_mfma_f32_32x32x16_f16 a[64:79], v[32:35], v[104:107], a[64:79]
	ds_read_b128 v[32:35], v98 offset:7168
	v_mfma_f32_32x32x16_f16 a[48:63], v[36:39], v[104:107], a[48:63]
	s_add_u32 m0, s47, 0xd3c0
	s_add_u32 s42, s42, 0x1800
	s_addc_u32 s43, s43, 0
	global_load_lds_dwordx4 v77, s[42:43]
	ds_read_b128 v[36:39], v98 offset:8192
	v_mfma_f32_32x32x16_f16 a[32:47], v[40:43], v[104:107], a[32:47]
	ds_read_b128 v[40:43], v98 offset:9216
	v_mfma_f32_32x32x16_f16 a[16:31], v[44:47], v[104:107], a[16:31]
	s_add_u32 m0, s48, 0xd3c0
	s_add_u32 s44, s44, 0x1800
	s_addc_u32 s45, s45, 0
	global_load_lds_dwordx4 v78, s[44:45]
	ds_read_b128 v[44:47], v98 offset:10240
	v_mfma_f32_32x32x16_f16 a[0:15], v[48:51], v[104:107], a[0:15]
	ds_read_b128 v[48:51], v98 offset:11264
	s_waitcnt lgkmcnt(6)
	v_mfma_f32_32x32x16_f16 a[80:95], v[4:7], v[108:111], a[80:95]
	s_waitcnt vmcnt(24)
	ds_write_b128 v81, v[132:135]
	ds_write_b128 v81, v[136:139] offset:1024
	v_mfma_f32_32x32x16_f16 a[64:79], v[8:11], v[108:111], a[64:79]
	ds_write_b128 v81, v[140:143] offset:2048
	ds_write_b128 v81, v[144:147] offset:3072
	v_mfma_f32_32x32x16_f16 a[48:63], v[12:15], v[108:111], a[48:63]
	ds_read_b128 v[52:55], v95
	ds_read_b128 v[56:59], v96
	ds_read_b128 v[60:63], v97
	ds_read_b128 v[0:3], v94
	v_mfma_f32_32x32x16_f16 a[32:47], v[16:19], v[108:111], a[32:47]
	s_waitcnt vmcnt(10)
	s_waitcnt lgkmcnt(8)
	s_barrier
	ds_read_b128 v[4:7], v84 offset:0
	ds_read_b128 v[8:11], v84 offset:1024
	ds_read_b128 v[12:15], v84 offset:2048
	ds_read_b128 v[16:19], v84 offset:3072
	v_mfma_f32_32x32x16_f16 a[16:31], v[20:23], v[108:111], a[16:31]
	ds_read_b128 v[20:23], v84 offset:4096
	v_mfma_f32_32x32x16_f16 a[0:15], v[24:27], v[108:111], a[0:15]
	ds_read_b128 v[24:27], v84 offset:5120
	s_waitcnt lgkmcnt(6)
	v_mfma_f32_32x32x16_f16 a[80:95], v[28:31], v[112:115], a[80:95]
	s_add_u32 m0, s46, 0x103c0
	s_add_u32 s40, s40, 0x1800
	s_addc_u32 s41, s41, 0
	global_load_lds_dwordx4 v76, s[40:41]
	ds_read_b128 v[28:31], v84 offset:6144
	v_mfma_f32_32x32x16_f16 a[64:79], v[32:35], v[112:115], a[64:79]
	global_load_dwordx4 v[132:135], v64, s[4:5] offset:896
	global_load_dwordx4 v[136:139], v66, s[4:5] offset:896
	ds_read_b128 v[32:35], v84 offset:7168
	v_mfma_f32_32x32x16_f16 a[48:63], v[36:39], v[112:115], a[48:63]
	s_add_u32 m0, s47, 0x103c0
	s_add_u32 s42, s42, 0x1800
	s_addc_u32 s43, s43, 0
	global_load_lds_dwordx4 v77, s[42:43]
	ds_read_b128 v[36:39], v84 offset:8192
	v_mfma_f32_32x32x16_f16 a[32:47], v[40:43], v[112:115], a[32:47]
	global_load_dwordx4 v[140:143], v68, s[4:5] offset:896
	global_load_dwordx4 v[144:147], v70, s[4:5] offset:896
	ds_read_b128 v[40:43], v84 offset:9216
	v_mfma_f32_32x32x16_f16 a[16:31], v[44:47], v[112:115], a[16:31]
	s_add_u32 m0, s48, 0x103c0
	s_add_u32 s44, s44, 0x1800
	s_addc_u32 s45, s45, 0
	global_load_lds_dwordx4 v78, s[44:45]
	ds_read_b128 v[44:47], v84 offset:10240
	v_mfma_f32_32x32x16_f16 a[0:15], v[48:51], v[112:115], a[0:15]
	ds_read_b128 v[48:51], v84 offset:11264
	s_waitcnt lgkmcnt(6)
	v_mfma_f32_32x32x16_f16 a[80:95], v[4:7], v[52:55], a[80:95]
	v_mfma_f32_32x32x16_f16 a[64:79], v[8:11], v[52:55], a[64:79]
	v_mfma_f32_32x32x16_f16 a[48:63], v[12:15], v[52:55], a[48:63]
	v_mfma_f32_32x32x16_f16 a[32:47], v[16:19], v[52:55], a[32:47]
	s_waitcnt vmcnt(10)
	s_waitcnt lgkmcnt(0)
	s_barrier
	ds_read_b128 v[4:7], v84 offset:12288
	ds_read_b128 v[8:11], v84 offset:13312
	ds_read_b128 v[12:15], v84 offset:14336
	ds_read_b128 v[16:19], v84 offset:15360
	v_mfma_f32_32x32x16_f16 a[16:31], v[20:23], v[52:55], a[16:31]
	ds_read_b128 v[20:23], v84 offset:16384
	v_mfma_f32_32x32x16_f16 a[0:15], v[24:27], v[52:55], a[0:15]
	ds_read_b128 v[24:27], v84 offset:17408
	v_mfma_f32_32x32x16_f16 a[80:95], v[28:31], v[56:59], a[80:95]
	s_add_u32 m0, s46, 0x0
	s_add_u32 s40, s40, 0x1800
	s_addc_u32 s41, s41, 0
	global_load_lds_dwordx4 v76, s[40:41]
	ds_read_b128 v[28:31], v84 offset:18432
	v_mfma_f32_32x32x16_f16 a[64:79], v[32:35], v[56:59], a[64:79]
	ds_read_b128 v[32:35], v84 offset:19456
	v_mfma_f32_32x32x16_f16 a[48:63], v[36:39], v[56:59], a[48:63]
	s_add_u32 m0, s47, 0x0
	s_add_u32 s42, s42, 0x1800
	s_addc_u32 s43, s43, 0
	global_load_lds_dwordx4 v77, s[42:43]
	ds_read_b128 v[36:39], v84 offset:20480
	v_mfma_f32_32x32x16_f16 a[32:47], v[40:43], v[56:59], a[32:47]
	ds_read_b128 v[40:43], v84 offset:21504
	v_mfma_f32_32x32x16_f16 a[16:31], v[44:47], v[56:59], a[16:31]
	s_add_u32 m0, s48, 0x0
	s_add_u32 s44, s44, 0x1800
	s_addc_u32 s45, s45, 0
	global_load_lds_dwordx4 v78, s[44:45]
	ds_read_b128 v[44:47], v84 offset:22528
	v_mfma_f32_32x32x16_f16 a[0:15], v[48:51], v[56:59], a[0:15]
	ds_read_b128 v[48:51], v84 offset:23552
	s_waitcnt lgkmcnt(6)
	v_mfma_f32_32x32x16_f16 a[80:95], v[4:7], v[60:63], a[80:95]
	s_waitcnt vmcnt(24)
	ds_write_b128 v81, v[148:151]
	ds_write_b128 v81, v[152:155] offset:1024
	v_mfma_f32_32x32x16_f16 a[64:79], v[8:11], v[60:63], a[64:79]
	ds_write_b128 v81, v[156:159] offset:2048
	ds_write_b128 v81, v[72:75] offset:3072
	v_mfma_f32_32x32x16_f16 a[48:63], v[12:15], v[60:63], a[48:63]
	ds_read_b128 v[100:103], v95
	ds_read_b128 v[104:107], v96
	ds_read_b128 v[108:111], v97
	ds_read_b128 v[112:115], v94
	v_mfma_f32_32x32x16_f16 a[32:47], v[16:19], v[60:63], a[32:47]
	s_waitcnt vmcnt(10)
	s_waitcnt lgkmcnt(8)
	s_barrier
	ds_read_b128 v[4:7], v84 offset:54208
	ds_read_b128 v[8:11], v84 offset:55232
	ds_read_b128 v[12:15], v84 offset:56256
	ds_read_b128 v[16:19], v84 offset:57280
	v_mfma_f32_32x32x16_f16 a[16:31], v[20:23], v[60:63], a[16:31]
	ds_read_b128 v[20:23], v84 offset:58304
	v_mfma_f32_32x32x16_f16 a[0:15], v[24:27], v[60:63], a[0:15]
	ds_read_b128 v[24:27], v84 offset:59328
	s_waitcnt lgkmcnt(6)
	v_mfma_f32_32x32x16_f16 a[80:95], v[28:31], v[0:3], a[80:95]
	s_add_u32 m0, s46, 0x3000
	s_add_u32 s40, s40, 0x1800
	s_addc_u32 s41, s41, 0
	global_load_lds_dwordx4 v76, s[40:41]
	ds_read_b128 v[28:31], v84 offset:60352
	v_mfma_f32_32x32x16_f16 a[64:79], v[32:35], v[0:3], a[64:79]
	global_load_dwordx4 v[148:151], v64, s[4:5] offset:1024
	global_load_dwordx4 v[152:155], v66, s[4:5] offset:1024
	ds_read_b128 v[32:35], v84 offset:61376
	v_mfma_f32_32x32x16_f16 a[48:63], v[36:39], v[0:3], a[48:63]
	s_add_u32 m0, s47, 0x3000
	s_add_u32 s42, s42, 0x1800
	s_addc_u32 s43, s43, 0
	global_load_lds_dwordx4 v77, s[42:43]
	ds_read_b128 v[36:39], v84 offset:62400
	v_mfma_f32_32x32x16_f16 a[32:47], v[40:43], v[0:3], a[32:47]
	global_load_dwordx4 v[156:159], v68, s[4:5] offset:1024
	global_load_dwordx4 v[72:75], v70, s[4:5] offset:1024
	ds_read_b128 v[40:43], v84 offset:63424
	v_mfma_f32_32x32x16_f16 a[16:31], v[44:47], v[0:3], a[16:31]
	s_add_u32 m0, s48, 0x3000
	s_add_u32 s44, s44, 0x1800
	s_addc_u32 s45, s45, 0
	global_load_lds_dwordx4 v78, s[44:45]
	ds_read_b128 v[44:47], v84 offset:64448
	v_mfma_f32_32x32x16_f16 a[0:15], v[48:51], v[0:3], a[0:15]
	ds_read_b128 v[48:51], v84 offset:65472
	s_waitcnt lgkmcnt(6)
	v_mfma_f32_32x32x16_f16 a[80:95], v[4:7], v[100:103], a[80:95]
	v_mfma_f32_32x32x16_f16 a[64:79], v[8:11], v[100:103], a[64:79]
	v_mfma_f32_32x32x16_f16 a[48:63], v[12:15], v[100:103], a[48:63]
	v_mfma_f32_32x32x16_f16 a[32:47], v[16:19], v[100:103], a[32:47]
	s_waitcnt vmcnt(10)
	s_waitcnt lgkmcnt(0)
	s_barrier
	ds_read_b128 v[4:7], v98
	ds_read_b128 v[8:11], v98 offset:1024
	ds_read_b128 v[12:15], v98 offset:2048
	ds_read_b128 v[16:19], v98 offset:3072
	v_mfma_f32_32x32x16_f16 a[16:31], v[20:23], v[100:103], a[16:31]
	ds_read_b128 v[20:23], v98 offset:4096
	v_mfma_f32_32x32x16_f16 a[0:15], v[24:27], v[100:103], a[0:15]
	ds_read_b128 v[24:27], v98 offset:5120
	v_mfma_f32_32x32x16_f16 a[80:95], v[28:31], v[104:107], a[80:95]
	s_add_u32 m0, s46, 0xd3c0
	s_add_u32 s40, s40, 0x1800
	s_addc_u32 s41, s41, 0
	global_load_lds_dwordx4 v76, s[40:41]
	ds_read_b128 v[28:31], v98 offset:6144
	v_mfma_f32_32x32x16_f16 a[64:79], v[32:35], v[104:107], a[64:79]
	ds_read_b128 v[32:35], v98 offset:7168
	v_mfma_f32_32x32x16_f16 a[48:63], v[36:39], v[104:107], a[48:63]
	s_add_u32 m0, s47, 0xd3c0
	s_add_u32 s42, s42, 0x1800
	s_addc_u32 s43, s43, 0
	global_load_lds_dwordx4 v77, s[42:43]
	ds_read_b128 v[36:39], v98 offset:8192
	v_mfma_f32_32x32x16_f16 a[32:47], v[40:43], v[104:107], a[32:47]
	ds_read_b128 v[40:43], v98 offset:9216
	v_mfma_f32_32x32x16_f16 a[16:31], v[44:47], v[104:107], a[16:31]
	s_add_u32 m0, s48, 0xd3c0
	s_add_u32 s44, s44, 0x1800
	s_addc_u32 s45, s45, 0
	global_load_lds_dwordx4 v78, s[44:45]
	ds_read_b128 v[44:47], v98 offset:10240
	v_mfma_f32_32x32x16_f16 a[0:15], v[48:51], v[104:107], a[0:15]
	ds_read_b128 v[48:51], v98 offset:11264
	s_waitcnt lgkmcnt(6)
	v_mfma_f32_32x32x16_f16 a[80:95], v[4:7], v[108:111], a[80:95]
	s_waitcnt vmcnt(24)
	ds_write_b128 v81, v[116:119]
	ds_write_b128 v81, v[120:123] offset:1024
	v_mfma_f32_32x32x16_f16 a[64:79], v[8:11], v[108:111], a[64:79]
	ds_write_b128 v81, v[124:127] offset:2048
	ds_write_b128 v81, v[128:131] offset:3072
	v_mfma_f32_32x32x16_f16 a[48:63], v[12:15], v[108:111], a[48:63]
	ds_read_b128 v[52:55], v95
	ds_read_b128 v[56:59], v96
	ds_read_b128 v[60:63], v97
	ds_read_b128 v[0:3], v94
	v_mfma_f32_32x32x16_f16 a[32:47], v[16:19], v[108:111], a[32:47]
	s_waitcnt vmcnt(10)
	s_waitcnt lgkmcnt(8)
	s_barrier
	ds_read_b128 v[4:7], v84 offset:0
	ds_read_b128 v[8:11], v84 offset:1024
	ds_read_b128 v[12:15], v84 offset:2048
	ds_read_b128 v[16:19], v84 offset:3072
	v_mfma_f32_32x32x16_f16 a[16:31], v[20:23], v[108:111], a[16:31]
	ds_read_b128 v[20:23], v84 offset:4096
	v_mfma_f32_32x32x16_f16 a[0:15], v[24:27], v[108:111], a[0:15]
	ds_read_b128 v[24:27], v84 offset:5120
	s_waitcnt lgkmcnt(6)
	v_mfma_f32_32x32x16_f16 a[80:95], v[28:31], v[112:115], a[80:95]
	s_add_u32 m0, s46, 0x103c0
	s_add_u32 s40, s40, 0x1800
	s_addc_u32 s41, s41, 0
	global_load_lds_dwordx4 v76, s[40:41]
	ds_read_b128 v[28:31], v84 offset:6144
	v_mfma_f32_32x32x16_f16 a[64:79], v[32:35], v[112:115], a[64:79]
	global_load_dwordx4 v[116:119], v64, s[4:5] offset:1152
	global_load_dwordx4 v[120:123], v66, s[4:5] offset:1152
	ds_read_b128 v[32:35], v84 offset:7168
	v_mfma_f32_32x32x16_f16 a[48:63], v[36:39], v[112:115], a[48:63]
	s_add_u32 m0, s47, 0x103c0
	s_add_u32 s42, s42, 0x1800
	s_addc_u32 s43, s43, 0
	global_load_lds_dwordx4 v77, s[42:43]
	ds_read_b128 v[36:39], v84 offset:8192
	v_mfma_f32_32x32x16_f16 a[32:47], v[40:43], v[112:115], a[32:47]
	global_load_dwordx4 v[124:127], v68, s[4:5] offset:1152
	global_load_dwordx4 v[128:131], v70, s[4:5] offset:1152
	ds_read_b128 v[40:43], v84 offset:9216
	v_mfma_f32_32x32x16_f16 a[16:31], v[44:47], v[112:115], a[16:31]
	s_add_u32 m0, s48, 0x103c0
	s_add_u32 s44, s44, 0x1800
	s_addc_u32 s45, s45, 0
	global_load_lds_dwordx4 v78, s[44:45]
	ds_read_b128 v[44:47], v84 offset:10240
	v_mfma_f32_32x32x16_f16 a[0:15], v[48:51], v[112:115], a[0:15]
	ds_read_b128 v[48:51], v84 offset:11264
	s_waitcnt lgkmcnt(6)
	v_mfma_f32_32x32x16_f16 a[80:95], v[4:7], v[52:55], a[80:95]
	v_mfma_f32_32x32x16_f16 a[64:79], v[8:11], v[52:55], a[64:79]
	v_mfma_f32_32x32x16_f16 a[48:63], v[12:15], v[52:55], a[48:63]
	v_mfma_f32_32x32x16_f16 a[32:47], v[16:19], v[52:55], a[32:47]
	s_waitcnt vmcnt(10)
	s_waitcnt lgkmcnt(0)
	s_barrier
	ds_read_b128 v[4:7], v84 offset:12288
	ds_read_b128 v[8:11], v84 offset:13312
	ds_read_b128 v[12:15], v84 offset:14336
	ds_read_b128 v[16:19], v84 offset:15360
	v_mfma_f32_32x32x16_f16 a[16:31], v[20:23], v[52:55], a[16:31]
	ds_read_b128 v[20:23], v84 offset:16384
	v_mfma_f32_32x32x16_f16 a[0:15], v[24:27], v[52:55], a[0:15]
	ds_read_b128 v[24:27], v84 offset:17408
	v_mfma_f32_32x32x16_f16 a[80:95], v[28:31], v[56:59], a[80:95]
	s_add_u32 m0, s46, 0x0
	s_add_u32 s40, s40, 0x1800
	s_addc_u32 s41, s41, 0
	global_load_lds_dwordx4 v76, s[40:41]
	ds_read_b128 v[28:31], v84 offset:18432
	v_mfma_f32_32x32x16_f16 a[64:79], v[32:35], v[56:59], a[64:79]
	ds_read_b128 v[32:35], v84 offset:19456
	v_mfma_f32_32x32x16_f16 a[48:63], v[36:39], v[56:59], a[48:63]
	s_add_u32 m0, s47, 0x0
	s_add_u32 s42, s42, 0x1800
	s_addc_u32 s43, s43, 0
	global_load_lds_dwordx4 v77, s[42:43]
	ds_read_b128 v[36:39], v84 offset:20480
	v_mfma_f32_32x32x16_f16 a[32:47], v[40:43], v[56:59], a[32:47]
	ds_read_b128 v[40:43], v84 offset:21504
	v_mfma_f32_32x32x16_f16 a[16:31], v[44:47], v[56:59], a[16:31]
	s_add_u32 m0, s48, 0x0
	s_add_u32 s44, s44, 0x1800
	s_addc_u32 s45, s45, 0
	global_load_lds_dwordx4 v78, s[44:45]
	ds_read_b128 v[44:47], v84 offset:22528
	v_mfma_f32_32x32x16_f16 a[0:15], v[48:51], v[56:59], a[0:15]
	ds_read_b128 v[48:51], v84 offset:23552
	s_waitcnt lgkmcnt(6)
	v_mfma_f32_32x32x16_f16 a[80:95], v[4:7], v[60:63], a[80:95]
	s_waitcnt vmcnt(24)
	ds_write_b128 v81, v[132:135]
	ds_write_b128 v81, v[136:139] offset:1024
	v_mfma_f32_32x32x16_f16 a[64:79], v[8:11], v[60:63], a[64:79]
	ds_write_b128 v81, v[140:143] offset:2048
	ds_write_b128 v81, v[144:147] offset:3072
	v_mfma_f32_32x32x16_f16 a[48:63], v[12:15], v[60:63], a[48:63]
	ds_read_b128 v[100:103], v95
	ds_read_b128 v[104:107], v96
	ds_read_b128 v[108:111], v97
	ds_read_b128 v[112:115], v94
	v_mfma_f32_32x32x16_f16 a[32:47], v[16:19], v[60:63], a[32:47]
	s_waitcnt vmcnt(10)
	s_waitcnt lgkmcnt(8)
	s_barrier
	ds_read_b128 v[4:7], v84 offset:54208
	ds_read_b128 v[8:11], v84 offset:55232
	ds_read_b128 v[12:15], v84 offset:56256
	ds_read_b128 v[16:19], v84 offset:57280
	v_mfma_f32_32x32x16_f16 a[16:31], v[20:23], v[60:63], a[16:31]
	ds_read_b128 v[20:23], v84 offset:58304
	v_mfma_f32_32x32x16_f16 a[0:15], v[24:27], v[60:63], a[0:15]
	ds_read_b128 v[24:27], v84 offset:59328
	s_waitcnt lgkmcnt(6)
	v_mfma_f32_32x32x16_f16 a[80:95], v[28:31], v[0:3], a[80:95]
	s_add_u32 m0, s46, 0x3000
	s_add_u32 s40, s40, 0x1800
	s_addc_u32 s41, s41, 0
	global_load_lds_dwordx4 v76, s[40:41]
	ds_read_b128 v[28:31], v84 offset:60352
	v_mfma_f32_32x32x16_f16 a[64:79], v[32:35], v[0:3], a[64:79]
	global_load_dwordx4 v[132:135], v64, s[4:5] offset:1280
	global_load_dwordx4 v[136:139], v66, s[4:5] offset:1280
	ds_read_b128 v[32:35], v84 offset:61376
	v_mfma_f32_32x32x16_f16 a[48:63], v[36:39], v[0:3], a[48:63]
	s_add_u32 m0, s47, 0x3000
	s_add_u32 s42, s42, 0x1800
	s_addc_u32 s43, s43, 0
	global_load_lds_dwordx4 v77, s[42:43]
	ds_read_b128 v[36:39], v84 offset:62400
	v_mfma_f32_32x32x16_f16 a[32:47], v[40:43], v[0:3], a[32:47]
	global_load_dwordx4 v[140:143], v68, s[4:5] offset:1280
	global_load_dwordx4 v[144:147], v70, s[4:5] offset:1280
	ds_read_b128 v[40:43], v84 offset:63424
	v_mfma_f32_32x32x16_f16 a[16:31], v[44:47], v[0:3], a[16:31]
	s_add_u32 m0, s48, 0x3000
	s_add_u32 s44, s44, 0x1800
	s_addc_u32 s45, s45, 0
	global_load_lds_dwordx4 v78, s[44:45]
	ds_read_b128 v[44:47], v84 offset:64448
	v_mfma_f32_32x32x16_f16 a[0:15], v[48:51], v[0:3], a[0:15]
	ds_read_b128 v[48:51], v84 offset:65472
	s_waitcnt lgkmcnt(6)
	v_mfma_f32_32x32x16_f16 a[80:95], v[4:7], v[100:103], a[80:95]
	v_mfma_f32_32x32x16_f16 a[64:79], v[8:11], v[100:103], a[64:79]
	v_mfma_f32_32x32x16_f16 a[48:63], v[12:15], v[100:103], a[48:63]
	v_mfma_f32_32x32x16_f16 a[32:47], v[16:19], v[100:103], a[32:47]
	s_waitcnt vmcnt(10)
	s_waitcnt lgkmcnt(0)
	s_barrier
	ds_read_b128 v[4:7], v98
	ds_read_b128 v[8:11], v98 offset:1024
	ds_read_b128 v[12:15], v98 offset:2048
	ds_read_b128 v[16:19], v98 offset:3072
	v_mfma_f32_32x32x16_f16 a[16:31], v[20:23], v[100:103], a[16:31]
	ds_read_b128 v[20:23], v98 offset:4096
	v_mfma_f32_32x32x16_f16 a[0:15], v[24:27], v[100:103], a[0:15]
	ds_read_b128 v[24:27], v98 offset:5120
	v_mfma_f32_32x32x16_f16 a[80:95], v[28:31], v[104:107], a[80:95]
	s_add_u32 m0, s46, 0xd3c0
	s_add_u32 s40, s40, 0x1800
	s_addc_u32 s41, s41, 0
	global_load_lds_dwordx4 v76, s[40:41]
	ds_read_b128 v[28:31], v98 offset:6144
	v_mfma_f32_32x32x16_f16 a[64:79], v[32:35], v[104:107], a[64:79]
	ds_read_b128 v[32:35], v98 offset:7168
	v_mfma_f32_32x32x16_f16 a[48:63], v[36:39], v[104:107], a[48:63]
	s_add_u32 m0, s47, 0xd3c0
	s_add_u32 s42, s42, 0x1800
	s_addc_u32 s43, s43, 0
	global_load_lds_dwordx4 v77, s[42:43]
	ds_read_b128 v[36:39], v98 offset:8192
	v_mfma_f32_32x32x16_f16 a[32:47], v[40:43], v[104:107], a[32:47]
	ds_read_b128 v[40:43], v98 offset:9216
	v_mfma_f32_32x32x16_f16 a[16:31], v[44:47], v[104:107], a[16:31]
	s_add_u32 m0, s48, 0xd3c0
	s_add_u32 s44, s44, 0x1800
	s_addc_u32 s45, s45, 0
	global_load_lds_dwordx4 v78, s[44:45]
	ds_read_b128 v[44:47], v98 offset:10240
	v_mfma_f32_32x32x16_f16 a[0:15], v[48:51], v[104:107], a[0:15]
	ds_read_b128 v[48:51], v98 offset:11264
	s_waitcnt lgkmcnt(6)
	v_mfma_f32_32x32x16_f16 a[80:95], v[4:7], v[108:111], a[80:95]
	s_waitcnt vmcnt(24)
	ds_write_b128 v81, v[148:151]
	ds_write_b128 v81, v[152:155] offset:1024
	v_mfma_f32_32x32x16_f16 a[64:79], v[8:11], v[108:111], a[64:79]
	ds_write_b128 v81, v[156:159] offset:2048
	ds_write_b128 v81, v[72:75] offset:3072
	v_mfma_f32_32x32x16_f16 a[48:63], v[12:15], v[108:111], a[48:63]
	ds_read_b128 v[52:55], v95
	ds_read_b128 v[56:59], v96
	ds_read_b128 v[60:63], v97
	ds_read_b128 v[0:3], v94
	v_mfma_f32_32x32x16_f16 a[32:47], v[16:19], v[108:111], a[32:47]
	s_waitcnt vmcnt(10)
	s_waitcnt lgkmcnt(8)
	s_barrier
	ds_read_b128 v[4:7], v84 offset:0
	ds_read_b128 v[8:11], v84 offset:1024
	ds_read_b128 v[12:15], v84 offset:2048
	ds_read_b128 v[16:19], v84 offset:3072
	v_mfma_f32_32x32x16_f16 a[16:31], v[20:23], v[108:111], a[16:31]
	ds_read_b128 v[20:23], v84 offset:4096
	v_mfma_f32_32x32x16_f16 a[0:15], v[24:27], v[108:111], a[0:15]
	ds_read_b128 v[24:27], v84 offset:5120
	s_waitcnt lgkmcnt(6)
	v_mfma_f32_32x32x16_f16 a[80:95], v[28:31], v[112:115], a[80:95]
	s_add_u32 m0, s46, 0x103c0
	s_add_u32 s40, s40, 0x1800
	s_addc_u32 s41, s41, 0
	global_load_lds_dwordx4 v76, s[40:41]
	ds_read_b128 v[28:31], v84 offset:6144
	v_mfma_f32_32x32x16_f16 a[64:79], v[32:35], v[112:115], a[64:79]
	global_load_dwordx4 v[148:151], v64, s[4:5] offset:1408
	global_load_dwordx4 v[152:155], v66, s[4:5] offset:1408
	ds_read_b128 v[32:35], v84 offset:7168
	v_mfma_f32_32x32x16_f16 a[48:63], v[36:39], v[112:115], a[48:63]
	s_add_u32 m0, s47, 0x103c0
	s_add_u32 s42, s42, 0x1800
	s_addc_u32 s43, s43, 0
	global_load_lds_dwordx4 v77, s[42:43]
	ds_read_b128 v[36:39], v84 offset:8192
	v_mfma_f32_32x32x16_f16 a[32:47], v[40:43], v[112:115], a[32:47]
	global_load_dwordx4 v[156:159], v68, s[4:5] offset:1408
	global_load_dwordx4 v[72:75], v70, s[4:5] offset:1408
	ds_read_b128 v[40:43], v84 offset:9216
	v_mfma_f32_32x32x16_f16 a[16:31], v[44:47], v[112:115], a[16:31]
	s_add_u32 m0, s48, 0x103c0
	s_add_u32 s44, s44, 0x1800
	s_addc_u32 s45, s45, 0
	global_load_lds_dwordx4 v78, s[44:45]
	ds_read_b128 v[44:47], v84 offset:10240
	v_mfma_f32_32x32x16_f16 a[0:15], v[48:51], v[112:115], a[0:15]
	ds_read_b128 v[48:51], v84 offset:11264
	s_waitcnt lgkmcnt(6)
	v_mfma_f32_32x32x16_f16 a[80:95], v[4:7], v[52:55], a[80:95]
	v_mfma_f32_32x32x16_f16 a[64:79], v[8:11], v[52:55], a[64:79]
	v_mfma_f32_32x32x16_f16 a[48:63], v[12:15], v[52:55], a[48:63]
	v_mfma_f32_32x32x16_f16 a[32:47], v[16:19], v[52:55], a[32:47]
	s_waitcnt vmcnt(10)
	s_waitcnt lgkmcnt(0)
	s_barrier
	ds_read_b128 v[4:7], v84 offset:12288
	ds_read_b128 v[8:11], v84 offset:13312
	ds_read_b128 v[12:15], v84 offset:14336
	ds_read_b128 v[16:19], v84 offset:15360
	v_mfma_f32_32x32x16_f16 a[16:31], v[20:23], v[52:55], a[16:31]
	ds_read_b128 v[20:23], v84 offset:16384
	v_mfma_f32_32x32x16_f16 a[0:15], v[24:27], v[52:55], a[0:15]
	ds_read_b128 v[24:27], v84 offset:17408
	v_mfma_f32_32x32x16_f16 a[80:95], v[28:31], v[56:59], a[80:95]
	s_add_u32 m0, s46, 0x0
	s_add_u32 s40, s40, 0x1800
	s_addc_u32 s41, s41, 0
	global_load_lds_dwordx4 v76, s[40:41]
	ds_read_b128 v[28:31], v84 offset:18432
	v_mfma_f32_32x32x16_f16 a[64:79], v[32:35], v[56:59], a[64:79]
	ds_read_b128 v[32:35], v84 offset:19456
	v_mfma_f32_32x32x16_f16 a[48:63], v[36:39], v[56:59], a[48:63]
	s_add_u32 m0, s47, 0x0
	s_add_u32 s42, s42, 0x1800
	s_addc_u32 s43, s43, 0
	global_load_lds_dwordx4 v77, s[42:43]
	ds_read_b128 v[36:39], v84 offset:20480
	v_mfma_f32_32x32x16_f16 a[32:47], v[40:43], v[56:59], a[32:47]
	ds_read_b128 v[40:43], v84 offset:21504
	v_mfma_f32_32x32x16_f16 a[16:31], v[44:47], v[56:59], a[16:31]
	s_add_u32 m0, s48, 0x0
	s_add_u32 s44, s44, 0x1800
	s_addc_u32 s45, s45, 0
	global_load_lds_dwordx4 v78, s[44:45]
	ds_read_b128 v[44:47], v84 offset:22528
	v_mfma_f32_32x32x16_f16 a[0:15], v[48:51], v[56:59], a[0:15]
	ds_read_b128 v[48:51], v84 offset:23552
	s_waitcnt lgkmcnt(6)
	v_mfma_f32_32x32x16_f16 a[80:95], v[4:7], v[60:63], a[80:95]
	s_waitcnt vmcnt(24)
	ds_write_b128 v81, v[116:119]
	ds_write_b128 v81, v[120:123] offset:1024
	v_mfma_f32_32x32x16_f16 a[64:79], v[8:11], v[60:63], a[64:79]
	ds_write_b128 v81, v[124:127] offset:2048
	ds_write_b128 v81, v[128:131] offset:3072
	v_mfma_f32_32x32x16_f16 a[48:63], v[12:15], v[60:63], a[48:63]
	ds_read_b128 v[100:103], v95
	ds_read_b128 v[104:107], v96
	ds_read_b128 v[108:111], v97
	ds_read_b128 v[112:115], v94
	v_mfma_f32_32x32x16_f16 a[32:47], v[16:19], v[60:63], a[32:47]
	s_waitcnt vmcnt(10)
	s_waitcnt lgkmcnt(8)
	s_barrier
	ds_read_b128 v[4:7], v84 offset:54208
	ds_read_b128 v[8:11], v84 offset:55232
	ds_read_b128 v[12:15], v84 offset:56256
	ds_read_b128 v[16:19], v84 offset:57280
	v_mfma_f32_32x32x16_f16 a[16:31], v[20:23], v[60:63], a[16:31]
	ds_read_b128 v[20:23], v84 offset:58304
	v_mfma_f32_32x32x16_f16 a[0:15], v[24:27], v[60:63], a[0:15]
	ds_read_b128 v[24:27], v84 offset:59328
	s_waitcnt lgkmcnt(6)
	v_mfma_f32_32x32x16_f16 a[80:95], v[28:31], v[0:3], a[80:95]
	s_add_u32 m0, s46, 0x3000
	s_add_u32 s40, s40, 0x1800
	s_addc_u32 s41, s41, 0
	global_load_lds_dwordx4 v76, s[40:41]
	ds_read_b128 v[28:31], v84 offset:60352
	v_mfma_f32_32x32x16_f16 a[64:79], v[32:35], v[0:3], a[64:79]
	global_load_dwordx4 v[116:119], v64, s[4:5] offset:1440
	global_load_dwordx4 v[120:123], v66, s[4:5] offset:1440
	ds_read_b128 v[32:35], v84 offset:61376
	v_mfma_f32_32x32x16_f16 a[48:63], v[36:39], v[0:3], a[48:63]
	s_add_u32 m0, s47, 0x3000
	s_add_u32 s42, s42, 0x1800
	s_addc_u32 s43, s43, 0
	global_load_lds_dwordx4 v77, s[42:43]
	ds_read_b128 v[36:39], v84 offset:62400
	v_mfma_f32_32x32x16_f16 a[32:47], v[40:43], v[0:3], a[32:47]
	global_load_dwordx4 v[124:127], v68, s[4:5] offset:1440
	global_load_dwordx4 v[128:131], v70, s[4:5] offset:1440
	ds_read_b128 v[40:43], v84 offset:63424
	v_mfma_f32_32x32x16_f16 a[16:31], v[44:47], v[0:3], a[16:31]
	s_add_u32 m0, s48, 0x3000
	s_add_u32 s44, s44, 0x1800
	s_addc_u32 s45, s45, 0
	global_load_lds_dwordx4 v78, s[44:45]
	ds_read_b128 v[44:47], v84 offset:64448
	v_mfma_f32_32x32x16_f16 a[0:15], v[48:51], v[0:3], a[0:15]
	ds_read_b128 v[48:51], v84 offset:65472
	s_waitcnt lgkmcnt(6)
	v_mfma_f32_32x32x16_f16 a[80:95], v[4:7], v[100:103], a[80:95]
	v_mfma_f32_32x32x16_f16 a[64:79], v[8:11], v[100:103], a[64:79]
	v_mfma_f32_32x32x16_f16 a[48:63], v[12:15], v[100:103], a[48:63]
	v_mfma_f32_32x32x16_f16 a[32:47], v[16:19], v[100:103], a[32:47]
	s_waitcnt vmcnt(10)
	s_waitcnt lgkmcnt(0)
	s_barrier
	ds_read_b128 v[4:7], v98
	ds_read_b128 v[8:11], v98 offset:1024
	ds_read_b128 v[12:15], v98 offset:2048
	ds_read_b128 v[16:19], v98 offset:3072
	v_mfma_f32_32x32x16_f16 a[16:31], v[20:23], v[100:103], a[16:31]
	ds_read_b128 v[20:23], v98 offset:4096
	v_mfma_f32_32x32x16_f16 a[0:15], v[24:27], v[100:103], a[0:15]
	ds_read_b128 v[24:27], v98 offset:5120
	v_mfma_f32_32x32x16_f16 a[80:95], v[28:31], v[104:107], a[80:95]
	s_add_u32 m0, s46, 0xd3c0
	s_add_u32 s40, s40, 0x1800
	s_addc_u32 s41, s41, 0
	global_load_lds_dwordx4 v76, s[40:41]
	ds_read_b128 v[28:31], v98 offset:6144
	v_mfma_f32_32x32x16_f16 a[64:79], v[32:35], v[104:107], a[64:79]
	ds_read_b128 v[32:35], v98 offset:7168
	v_mfma_f32_32x32x16_f16 a[48:63], v[36:39], v[104:107], a[48:63]
	s_add_u32 m0, s47, 0xd3c0
	s_add_u32 s42, s42, 0x1800
	s_addc_u32 s43, s43, 0
	global_load_lds_dwordx4 v77, s[42:43]
	ds_read_b128 v[36:39], v98 offset:8192
	v_mfma_f32_32x32x16_f16 a[32:47], v[40:43], v[104:107], a[32:47]
	ds_read_b128 v[40:43], v98 offset:9216
	v_mfma_f32_32x32x16_f16 a[16:31], v[44:47], v[104:107], a[16:31]
	s_add_u32 m0, s48, 0xd3c0
	s_add_u32 s44, s44, 0x1800
	s_addc_u32 s45, s45, 0
	global_load_lds_dwordx4 v78, s[44:45]
	ds_read_b128 v[44:47], v98 offset:10240
	v_mfma_f32_32x32x16_f16 a[0:15], v[48:51], v[104:107], a[0:15]
	ds_read_b128 v[48:51], v98 offset:11264
	s_waitcnt lgkmcnt(6)
	v_mfma_f32_32x32x16_f16 a[80:95], v[4:7], v[108:111], a[80:95]
	s_waitcnt vmcnt(24)
	ds_write_b128 v81, v[132:135]
	ds_write_b128 v81, v[136:139] offset:1024
	v_mfma_f32_32x32x16_f16 a[64:79], v[8:11], v[108:111], a[64:79]
	ds_write_b128 v81, v[140:143] offset:2048
	ds_write_b128 v81, v[144:147] offset:3072
	v_mfma_f32_32x32x16_f16 a[48:63], v[12:15], v[108:111], a[48:63]
	ds_read_b128 v[52:55], v95
	ds_read_b128 v[56:59], v96
	ds_read_b128 v[60:63], v97
	ds_read_b128 v[0:3], v94
	v_mfma_f32_32x32x16_f16 a[32:47], v[16:19], v[108:111], a[32:47]
	s_waitcnt vmcnt(10)
	s_waitcnt lgkmcnt(8)
	s_barrier
	ds_read_b128 v[4:7], v84 offset:0
	ds_read_b128 v[8:11], v84 offset:1024
	ds_read_b128 v[12:15], v84 offset:2048
	ds_read_b128 v[16:19], v84 offset:3072
	v_mfma_f32_32x32x16_f16 a[16:31], v[20:23], v[108:111], a[16:31]
	ds_read_b128 v[20:23], v84 offset:4096
	v_mfma_f32_32x32x16_f16 a[0:15], v[24:27], v[108:111], a[0:15]
	ds_read_b128 v[24:27], v84 offset:5120
	s_waitcnt lgkmcnt(6)
	v_mfma_f32_32x32x16_f16 a[80:95], v[28:31], v[112:115], a[80:95]
	s_add_u32 m0, s46, 0x103c0
	s_add_u32 s40, s40, 0x1800
	s_addc_u32 s41, s41, 0
	global_load_lds_dwordx4 v76, s[40:41]
	ds_read_b128 v[28:31], v84 offset:6144
	v_mfma_f32_32x32x16_f16 a[64:79], v[32:35], v[112:115], a[64:79]
	ds_read_b128 v[32:35], v84 offset:7168
	v_mfma_f32_32x32x16_f16 a[48:63], v[36:39], v[112:115], a[48:63]
	s_add_u32 m0, s47, 0x103c0
	s_add_u32 s42, s42, 0x1800
	s_addc_u32 s43, s43, 0
	global_load_lds_dwordx4 v77, s[42:43]
	ds_read_b128 v[36:39], v84 offset:8192
	v_mfma_f32_32x32x16_f16 a[32:47], v[40:43], v[112:115], a[32:47]
	ds_read_b128 v[40:43], v84 offset:9216
	v_mfma_f32_32x32x16_f16 a[16:31], v[44:47], v[112:115], a[16:31]
	s_add_u32 m0, s48, 0x103c0
	s_add_u32 s44, s44, 0x1800
	s_addc_u32 s45, s45, 0
	global_load_lds_dwordx4 v78, s[44:45]
	ds_read_b128 v[44:47], v84 offset:10240
	v_mfma_f32_32x32x16_f16 a[0:15], v[48:51], v[112:115], a[0:15]
	ds_read_b128 v[48:51], v84 offset:11264
	s_waitcnt lgkmcnt(6)
	v_mfma_f32_32x32x16_f16 a[80:95], v[4:7], v[52:55], a[80:95]
	v_mfma_f32_32x32x16_f16 a[64:79], v[8:11], v[52:55], a[64:79]
	v_mfma_f32_32x32x16_f16 a[48:63], v[12:15], v[52:55], a[48:63]
	v_mfma_f32_32x32x16_f16 a[32:47], v[16:19], v[52:55], a[32:47]
	s_waitcnt vmcnt(6)
	s_waitcnt lgkmcnt(0)
	s_barrier
	ds_read_b128 v[4:7], v84 offset:12288
	ds_read_b128 v[8:11], v84 offset:13312
	ds_read_b128 v[12:15], v84 offset:14336
	ds_read_b128 v[16:19], v84 offset:15360
	v_mfma_f32_32x32x16_f16 a[16:31], v[20:23], v[52:55], a[16:31]
	ds_read_b128 v[20:23], v84 offset:16384
	v_mfma_f32_32x32x16_f16 a[0:15], v[24:27], v[52:55], a[0:15]
	ds_read_b128 v[24:27], v84 offset:17408
	v_mfma_f32_32x32x16_f16 a[80:95], v[28:31], v[56:59], a[80:95]
	s_add_u32 m0, s46, 0x0
	s_add_u32 s40, s40, 0x1800
	s_addc_u32 s41, s41, 0
	global_load_lds_dwordx4 v76, s[40:41]
	ds_read_b128 v[28:31], v84 offset:18432
	v_mfma_f32_32x32x16_f16 a[64:79], v[32:35], v[56:59], a[64:79]
	ds_read_b128 v[32:35], v84 offset:19456
	v_mfma_f32_32x32x16_f16 a[48:63], v[36:39], v[56:59], a[48:63]
	s_add_u32 m0, s47, 0x0
	s_add_u32 s42, s42, s49
	s_addc_u32 s43, s43, 0
	global_load_lds_dwordx4 v77, s[42:43]
	ds_read_b128 v[36:39], v84 offset:20480
	v_mfma_f32_32x32x16_f16 a[32:47], v[40:43], v[56:59], a[32:47]
	ds_read_b128 v[40:43], v84 offset:21504
	v_mfma_f32_32x32x16_f16 a[16:31], v[44:47], v[56:59], a[16:31]
	s_add_u32 m0, s48, 0x0
	s_add_u32 s44, s44, 0xc00
	s_addc_u32 s45, s45, 0
	global_load_lds_dwordx4 v78, s[44:45]
	ds_read_b128 v[44:47], v84 offset:22528
	v_mfma_f32_32x32x16_f16 a[0:15], v[48:51], v[56:59], a[0:15]
	ds_read_b128 v[48:51], v84 offset:23552
	s_waitcnt lgkmcnt(6)
	v_mfma_f32_32x32x16_f16 a[80:95], v[4:7], v[60:63], a[80:95]
	s_waitcnt vmcnt(20)
	ds_write_b128 v81, v[148:151]
	ds_write_b128 v81, v[152:155] offset:1024
	v_mfma_f32_32x32x16_f16 a[64:79], v[8:11], v[60:63], a[64:79]
	ds_write_b128 v81, v[156:159] offset:2048
	ds_write_b128 v81, v[72:75] offset:3072
	v_mfma_f32_32x32x16_f16 a[48:63], v[12:15], v[60:63], a[48:63]
	ds_read_b128 v[100:103], v95
	ds_read_b128 v[104:107], v96
	ds_read_b128 v[108:111], v97
	ds_read_b128 v[112:115], v94
	v_mfma_f32_32x32x16_f16 a[32:47], v[16:19], v[60:63], a[32:47]
	s_waitcnt vmcnt(6)
	s_waitcnt lgkmcnt(8)
	s_barrier
	ds_read_b128 v[4:7], v84 offset:54208
	ds_read_b128 v[8:11], v84 offset:55232
	ds_read_b128 v[12:15], v84 offset:56256
	ds_read_b128 v[16:19], v84 offset:57280
	v_mfma_f32_32x32x16_f16 a[16:31], v[20:23], v[60:63], a[16:31]
	ds_read_b128 v[20:23], v84 offset:58304
	v_mfma_f32_32x32x16_f16 a[0:15], v[24:27], v[60:63], a[0:15]
	ds_read_b128 v[24:27], v84 offset:59328
	s_waitcnt lgkmcnt(6)
	v_mfma_f32_32x32x16_f16 a[80:95], v[28:31], v[0:3], a[80:95]
	ds_read_b128 v[28:31], v84 offset:60352
	v_mfma_f32_32x32x16_f16 a[64:79], v[32:35], v[0:3], a[64:79]
	ds_read_b128 v[32:35], v84 offset:61376
	v_mfma_f32_32x32x16_f16 a[48:63], v[36:39], v[0:3], a[48:63]
	ds_read_b128 v[36:39], v84 offset:62400
	v_mfma_f32_32x32x16_f16 a[32:47], v[40:43], v[0:3], a[32:47]
	ds_read_b128 v[40:43], v84 offset:63424
	v_mfma_f32_32x32x16_f16 a[16:31], v[44:47], v[0:3], a[16:31]
	ds_read_b128 v[44:47], v84 offset:64448
	v_mfma_f32_32x32x16_f16 a[0:15], v[48:51], v[0:3], a[0:15]
	ds_read_b128 v[48:51], v84 offset:65472
	s_waitcnt lgkmcnt(6)
	v_mfma_f32_32x32x16_f16 a[80:95], v[4:7], v[100:103], a[80:95]
	v_mfma_f32_32x32x16_f16 a[64:79], v[8:11], v[100:103], a[64:79]
	v_mfma_f32_32x32x16_f16 a[48:63], v[12:15], v[100:103], a[48:63]
	v_mfma_f32_32x32x16_f16 a[32:47], v[16:19], v[100:103], a[32:47]
	s_waitcnt vmcnt(3)
	s_waitcnt lgkmcnt(0)
	s_barrier
	ds_read_b128 v[4:7], v98
	ds_read_b128 v[8:11], v98 offset:1024
	ds_read_b128 v[12:15], v98 offset:2048
	ds_read_b128 v[16:19], v98 offset:3072
	v_mfma_f32_32x32x16_f16 a[16:31], v[20:23], v[100:103], a[16:31]
	ds_read_b128 v[20:23], v98 offset:4096
	v_mfma_f32_32x32x16_f16 a[0:15], v[24:27], v[100:103], a[0:15]
	ds_read_b128 v[24:27], v98 offset:5120
	v_mfma_f32_32x32x16_f16 a[80:95], v[28:31], v[104:107], a[80:95]
	ds_read_b128 v[28:31], v98 offset:6144
	v_mfma_f32_32x32x16_f16 a[64:79], v[32:35], v[104:107], a[64:79]
	ds_read_b128 v[32:35], v98 offset:7168
	v_mfma_f32_32x32x16_f16 a[48:63], v[36:39], v[104:107], a[48:63]
	ds_read_b128 v[36:39], v98 offset:8192
	v_mfma_f32_32x32x16_f16 a[32:47], v[40:43], v[104:107], a[32:47]
	ds_read_b128 v[40:43], v98 offset:9216
	v_mfma_f32_32x32x16_f16 a[16:31], v[44:47], v[104:107], a[16:31]
	ds_read_b128 v[44:47], v98 offset:10240
	v_mfma_f32_32x32x16_f16 a[0:15], v[48:51], v[104:107], a[0:15]
	ds_read_b128 v[48:51], v98 offset:11264
	s_waitcnt lgkmcnt(6)
	v_mfma_f32_32x32x16_f16 a[80:95], v[4:7], v[108:111], a[80:95]
	s_waitcnt vmcnt(10)
	ds_write_b128 v81, v[116:119]
	ds_write_b128 v81, v[120:123] offset:1024
	v_mfma_f32_32x32x16_f16 a[64:79], v[8:11], v[108:111], a[64:79]
	ds_write_b128 v81, v[124:127] offset:2048
	ds_write_b128 v81, v[128:131] offset:3072
	v_mfma_f32_32x32x16_f16 a[48:63], v[12:15], v[108:111], a[48:63]
	ds_read_b128 v[0:3], v94
	v_mfma_f32_32x32x16_f16 a[32:47], v[16:19], v[108:111], a[32:47]
	s_waitcnt vmcnt(0)
	s_waitcnt lgkmcnt(5)
	s_barrier
	ds_read_b128 v[4:7], v84 offset:0
	ds_read_b128 v[8:11], v84 offset:1024
	ds_read_b128 v[12:15], v84 offset:2048
	ds_read_b128 v[16:19], v84 offset:3072
	v_mfma_f32_32x32x16_f16 a[16:31], v[20:23], v[108:111], a[16:31]
	ds_read_b128 v[20:23], v84 offset:4096
	v_mfma_f32_32x32x16_f16 a[0:15], v[24:27], v[108:111], a[0:15]
	ds_read_b128 v[24:27], v84 offset:5120
	s_waitcnt lgkmcnt(6)
	v_mfma_f32_32x32x16_f16 a[80:95], v[28:31], v[112:115], a[80:95]
	v_mfma_f32_32x32x16_f16 a[64:79], v[32:35], v[112:115], a[64:79]
	v_mfma_f32_32x32x16_f16 a[48:63], v[36:39], v[112:115], a[48:63]
	v_mfma_f32_32x32x16_f16 a[32:47], v[40:43], v[112:115], a[32:47]
	v_mfma_f32_32x32x16_f16 a[16:31], v[44:47], v[112:115], a[16:31]
	v_mfma_f32_32x32x16_f16 a[0:15], v[48:51], v[112:115], a[0:15]
	s_waitcnt lgkmcnt(0)
	v_mfma_f32_32x32x16_f16 a[80:95], v[4:7], v[0:3], a[80:95]
	v_mfma_f32_32x32x16_f16 a[16:31], v[20:23], v[0:3], a[16:31]
	v_lshlrev_b32_e32 v22, 4, v85
	v_mfma_f32_32x32x16_f16 a[64:79], v[8:11], v[0:3], a[64:79]
	v_mfma_f32_32x32x16_f16 a[48:63], v[12:15], v[0:3], a[48:63]
	s_nop 7
	v_accvgpr_read_b32 v13, a88
	v_mfma_f32_32x32x16_f16 a[32:47], v[16:19], v[0:3], a[32:47]
	v_accvgpr_read_b32 v17, a92
	v_mfma_f32_32x32x16_f16 a[0:15], v[24:27], v[0:3], a[0:15]
	ds_read_b128 v[2:5], v22 offset:53248
	ds_read_b128 v[6:9], v22 offset:53280
	v_accvgpr_read_b32 v1, a80
	v_lshlrev_b32_e32 v0, 4, v92
	s_waitcnt lgkmcnt(1)
	v_add_f32_e32 v1, v1, v2
	v_accvgpr_read_b32 v2, a81
	v_add_f32_e32 v2, v3, v2
	v_max_f32_e32 v10, 0, v2
	v_accvgpr_read_b32 v2, a82
	v_add_f32_e32 v2, v4, v2
	v_max_f32_e32 v11, 0, v2
	v_accvgpr_read_b32 v2, a83
	v_add_f32_e32 v2, v5, v2
	v_max_f32_e32 v12, 0, v2
	v_accvgpr_read_b32 v2, a84
	s_waitcnt lgkmcnt(0)
	v_add_f32_e32 v2, v2, v6
	v_max_f32_e32 v6, 0, v2
	v_accvgpr_read_b32 v2, a85
	v_add_f32_e32 v2, v7, v2
	v_max_f32_e32 v7, 0, v2
	v_accvgpr_read_b32 v2, a86
	v_add_f32_e32 v2, v8, v2
	v_max_f32_e32 v8, 0, v2
	v_accvgpr_read_b32 v2, a87
	v_add_f32_e32 v2, v9, v2
	v_max_f32_e32 v9, 0, v2
	ds_read_b128 v[2:5], v22 offset:53312
	v_max_f32_e32 v1, 0, v1
	s_waitcnt lgkmcnt(0)
	v_add_f32_e32 v2, v13, v2
	v_max_f32_e32 v13, 0, v2
	v_accvgpr_read_b32 v2, a89
	v_add_f32_e32 v2, v3, v2
	v_max_f32_e32 v14, 0, v2
	v_accvgpr_read_b32 v2, a90
	v_add_f32_e32 v2, v4, v2
	v_max_f32_e32 v15, 0, v2
	v_accvgpr_read_b32 v2, a91
	v_add_f32_e32 v2, v5, v2
	v_max_f32_e32 v16, 0, v2
	ds_read_b128 v[2:5], v22 offset:53344
	s_waitcnt lgkmcnt(0)
	v_add_f32_e32 v2, v17, v2
	v_max_f32_e32 v17, 0, v2
	v_accvgpr_read_b32 v2, a93
	v_add_f32_e32 v2, v3, v2
	v_max_f32_e32 v18, 0, v2
	v_accvgpr_read_b32 v2, a94
	v_add_f32_e32 v2, v4, v2
	v_max_f32_e32 v19, 0, v2
	v_accvgpr_read_b32 v2, a95
	v_add_f32_e32 v2, v5, v2
	v_cvt_pk_f16_f32 v5, v8, v9
	v_cvt_pk_f16_f32 v4, v6, v7
	ds_read_b128 v[6:9], v0 offset:40960
	v_max_f32_e32 v20, 0, v2
	v_cvt_pk_f16_f32 v3, v11, v12
	v_cvt_pk_f16_f32 v2, v1, v10
	v_accvgpr_read_b32 v1, a64
	s_waitcnt lgkmcnt(0)
	v_mfma_f32_32x32x16_f16 a[80:95], v[6:9], v[2:5], 0
	ds_read_b128 v[6:9], v0 offset:41984
	v_cvt_pk_f16_f32 v5, v19, v20
	v_cvt_pk_f16_f32 v4, v17, v18
	v_cvt_pk_f16_f32 v3, v15, v16
	v_cvt_pk_f16_f32 v2, v13, v14
	v_accvgpr_read_b32 v13, a72
	v_accvgpr_read_b32 v17, a76
	s_waitcnt lgkmcnt(0)
	v_mfma_f32_32x32x16_f16 a[80:95], v[6:9], v[2:5], a[80:95]
	ds_read_b128 v[2:5], v22 offset:53376
	v_accvgpr_read_b32 v9, a68
	s_waitcnt lgkmcnt(0)
	v_add_f32_e32 v1, v1, v2
	v_accvgpr_read_b32 v2, a65
	v_add_f32_e32 v2, v3, v2
	v_max_f32_e32 v6, 0, v2
	v_accvgpr_read_b32 v2, a66
	v_add_f32_e32 v2, v4, v2
	v_max_f32_e32 v7, 0, v2
	v_accvgpr_read_b32 v2, a67
	v_add_f32_e32 v2, v5, v2
	v_max_f32_e32 v8, 0, v2
	ds_read_b128 v[2:5], v22 offset:53408
	v_max_f32_e32 v1, 0, v1
	s_waitcnt lgkmcnt(0)
	v_add_f32_e32 v2, v9, v2
	v_max_f32_e32 v9, 0, v2
	v_accvgpr_read_b32 v2, a69
	v_add_f32_e32 v2, v3, v2
	v_max_f32_e32 v10, 0, v2
	v_accvgpr_read_b32 v2, a70
	v_add_f32_e32 v2, v4, v2
	v_max_f32_e32 v11, 0, v2
	v_accvgpr_read_b32 v2, a71
	v_add_f32_e32 v2, v5, v2
	v_max_f32_e32 v12, 0, v2
	ds_read_b128 v[2:5], v22 offset:53440
	s_waitcnt lgkmcnt(0)
	v_add_f32_e32 v2, v13, v2
	v_max_f32_e32 v13, 0, v2
	v_accvgpr_read_b32 v2, a73
	v_add_f32_e32 v2, v3, v2
	v_max_f32_e32 v14, 0, v2
	v_accvgpr_read_b32 v2, a74
	v_add_f32_e32 v2, v4, v2
	v_max_f32_e32 v15, 0, v2
	v_accvgpr_read_b32 v2, a75
	v_add_f32_e32 v2, v5, v2
	v_max_f32_e32 v16, 0, v2
	ds_read_b128 v[2:5], v22 offset:53472
	s_waitcnt lgkmcnt(0)
	v_add_f32_e32 v2, v17, v2
	v_max_f32_e32 v17, 0, v2
	v_accvgpr_read_b32 v2, a77
	v_add_f32_e32 v2, v3, v2
	v_max_f32_e32 v18, 0, v2
	v_accvgpr_read_b32 v2, a78
	v_add_f32_e32 v2, v4, v2
	v_max_f32_e32 v19, 0, v2
	v_accvgpr_read_b32 v2, a79
	v_add_f32_e32 v2, v5, v2
	v_max_f32_e32 v20, 0, v2
	v_cvt_pk_f16_f32 v4, v9, v10
	v_cvt_pk_f16_f32 v3, v7, v8
	v_cvt_pk_f16_f32 v2, v1, v6
	ds_read_b128 v[6:9], v0 offset:43008
	v_cvt_pk_f16_f32 v5, v11, v12
	v_accvgpr_read_b32 v1, a48
	s_waitcnt lgkmcnt(0)
	v_mfma_f32_32x32x16_f16 a[80:95], v[6:9], v[2:5], a[80:95]
	ds_read_b128 v[6:9], v0 offset:44032
	v_cvt_pk_f16_f32 v5, v19, v20
	v_cvt_pk_f16_f32 v4, v17, v18
	v_cvt_pk_f16_f32 v3, v15, v16
	v_cvt_pk_f16_f32 v2, v13, v14
	v_accvgpr_read_b32 v13, a56
	v_accvgpr_read_b32 v17, a60
	s_waitcnt lgkmcnt(0)
	v_mfma_f32_32x32x16_f16 a[80:95], v[6:9], v[2:5], a[80:95]
	ds_read_b128 v[2:5], v22 offset:53504
	v_accvgpr_read_b32 v9, a52
	s_waitcnt lgkmcnt(0)
	v_add_f32_e32 v1, v1, v2
	v_accvgpr_read_b32 v2, a49
	v_add_f32_e32 v2, v3, v2
	v_max_f32_e32 v6, 0, v2
	v_accvgpr_read_b32 v2, a50
	v_add_f32_e32 v2, v4, v2
	v_max_f32_e32 v7, 0, v2
	v_accvgpr_read_b32 v2, a51
	v_add_f32_e32 v2, v5, v2
	v_max_f32_e32 v8, 0, v2
	ds_read_b128 v[2:5], v22 offset:53536
	v_max_f32_e32 v1, 0, v1
	s_waitcnt lgkmcnt(0)
	v_add_f32_e32 v2, v9, v2
	v_max_f32_e32 v9, 0, v2
	v_accvgpr_read_b32 v2, a53
	v_add_f32_e32 v2, v3, v2
	v_max_f32_e32 v10, 0, v2
	v_accvgpr_read_b32 v2, a54
	v_add_f32_e32 v2, v4, v2
	v_max_f32_e32 v11, 0, v2
	v_accvgpr_read_b32 v2, a55
	v_add_f32_e32 v2, v5, v2
	v_max_f32_e32 v12, 0, v2
	ds_read_b128 v[2:5], v22 offset:53568
	s_waitcnt lgkmcnt(0)
	v_add_f32_e32 v2, v13, v2
	v_max_f32_e32 v13, 0, v2
	v_accvgpr_read_b32 v2, a57
	v_add_f32_e32 v2, v3, v2
	v_max_f32_e32 v14, 0, v2
	v_accvgpr_read_b32 v2, a58
	v_add_f32_e32 v2, v4, v2
	v_max_f32_e32 v15, 0, v2
	v_accvgpr_read_b32 v2, a59
	v_add_f32_e32 v2, v5, v2
	v_max_f32_e32 v16, 0, v2
	ds_read_b128 v[2:5], v22 offset:53600
	s_waitcnt lgkmcnt(0)
	v_add_f32_e32 v2, v17, v2
	v_max_f32_e32 v17, 0, v2
	v_accvgpr_read_b32 v2, a61
	v_add_f32_e32 v2, v3, v2
	v_max_f32_e32 v18, 0, v2
	v_accvgpr_read_b32 v2, a62
	v_add_f32_e32 v2, v4, v2
	v_max_f32_e32 v19, 0, v2
	v_accvgpr_read_b32 v2, a63
	v_add_f32_e32 v2, v5, v2
	v_max_f32_e32 v20, 0, v2
	v_cvt_pk_f16_f32 v4, v9, v10
	v_cvt_pk_f16_f32 v3, v7, v8
	v_cvt_pk_f16_f32 v2, v1, v6
	ds_read_b128 v[6:9], v0 offset:45056
	v_cvt_pk_f16_f32 v5, v11, v12
	v_accvgpr_read_b32 v1, a32
	s_waitcnt lgkmcnt(0)
	v_mfma_f32_32x32x16_f16 a[80:95], v[6:9], v[2:5], a[80:95]
	ds_read_b128 v[6:9], v0 offset:46080
	v_cvt_pk_f16_f32 v5, v19, v20
	v_cvt_pk_f16_f32 v4, v17, v18
	v_cvt_pk_f16_f32 v3, v15, v16
	v_cvt_pk_f16_f32 v2, v13, v14
	v_accvgpr_read_b32 v13, a40
	v_accvgpr_read_b32 v17, a44
	s_waitcnt lgkmcnt(0)
	v_mfma_f32_32x32x16_f16 a[80:95], v[6:9], v[2:5], a[80:95]
	ds_read_b128 v[2:5], v22 offset:53632
	v_accvgpr_read_b32 v9, a36
	s_waitcnt lgkmcnt(0)
	v_add_f32_e32 v1, v1, v2
	v_accvgpr_read_b32 v2, a33
	v_add_f32_e32 v2, v3, v2
	v_max_f32_e32 v6, 0, v2
	v_accvgpr_read_b32 v2, a34
	v_add_f32_e32 v2, v4, v2
	v_max_f32_e32 v7, 0, v2
	v_accvgpr_read_b32 v2, a35
	v_add_f32_e32 v2, v5, v2
	v_max_f32_e32 v8, 0, v2
	ds_read_b128 v[2:5], v22 offset:53664
	v_max_f32_e32 v1, 0, v1
	s_waitcnt lgkmcnt(0)
	v_add_f32_e32 v2, v9, v2
	v_max_f32_e32 v9, 0, v2
	v_accvgpr_read_b32 v2, a37
	v_add_f32_e32 v2, v3, v2
	v_max_f32_e32 v10, 0, v2
	v_accvgpr_read_b32 v2, a38
	v_add_f32_e32 v2, v4, v2
	v_max_f32_e32 v11, 0, v2
	v_accvgpr_read_b32 v2, a39
	v_add_f32_e32 v2, v5, v2
	v_max_f32_e32 v12, 0, v2
	ds_read_b128 v[2:5], v22 offset:53696
	s_waitcnt lgkmcnt(0)
	v_add_f32_e32 v2, v13, v2
	v_max_f32_e32 v13, 0, v2
	v_accvgpr_read_b32 v2, a41
	v_add_f32_e32 v2, v3, v2
	v_max_f32_e32 v14, 0, v2
	v_accvgpr_read_b32 v2, a42
	v_add_f32_e32 v2, v4, v2
	v_max_f32_e32 v15, 0, v2
	v_accvgpr_read_b32 v2, a43
	v_add_f32_e32 v2, v5, v2
	v_max_f32_e32 v16, 0, v2
	ds_read_b128 v[2:5], v22 offset:53728
	s_waitcnt lgkmcnt(0)
	v_add_f32_e32 v2, v17, v2
	v_max_f32_e32 v17, 0, v2
	v_accvgpr_read_b32 v2, a45
	v_add_f32_e32 v2, v3, v2
	v_max_f32_e32 v18, 0, v2
	v_accvgpr_read_b32 v2, a46
	v_add_f32_e32 v2, v4, v2
	v_max_f32_e32 v19, 0, v2
	v_accvgpr_read_b32 v2, a47
	v_add_f32_e32 v2, v5, v2
	v_max_f32_e32 v20, 0, v2
	v_cvt_pk_f16_f32 v4, v9, v10
	v_cvt_pk_f16_f32 v3, v7, v8
	v_cvt_pk_f16_f32 v2, v1, v6
	ds_read_b128 v[6:9], v0 offset:47104
	v_cvt_pk_f16_f32 v5, v11, v12
	v_accvgpr_read_b32 v1, a16
	s_waitcnt lgkmcnt(0)
	v_mfma_f32_32x32x16_f16 a[32:47], v[6:9], v[2:5], 0
	ds_read_b128 v[6:9], v0 offset:48128
	v_cvt_pk_f16_f32 v5, v19, v20
	v_cvt_pk_f16_f32 v4, v17, v18
	v_cvt_pk_f16_f32 v3, v15, v16
	v_cvt_pk_f16_f32 v2, v13, v14
	v_accvgpr_read_b32 v13, a24
	v_accvgpr_read_b32 v17, a28
	s_waitcnt lgkmcnt(0)
	v_mfma_f32_32x32x16_f16 a[32:47], v[6:9], v[2:5], a[32:47]
	ds_read_b128 v[2:5], v22 offset:53760
	v_accvgpr_read_b32 v9, a20
	s_waitcnt lgkmcnt(0)
	v_add_f32_e32 v1, v1, v2
	v_accvgpr_read_b32 v2, a17
	v_add_f32_e32 v2, v3, v2
	v_max_f32_e32 v6, 0, v2
	v_accvgpr_read_b32 v2, a18
	v_add_f32_e32 v2, v4, v2
	v_max_f32_e32 v7, 0, v2
	v_accvgpr_read_b32 v2, a19
	v_add_f32_e32 v2, v5, v2
	v_max_f32_e32 v8, 0, v2
	ds_read_b128 v[2:5], v22 offset:53792
	v_max_f32_e32 v1, 0, v1
	s_waitcnt lgkmcnt(0)
	v_add_f32_e32 v2, v9, v2
	v_max_f32_e32 v9, 0, v2
	v_accvgpr_read_b32 v2, a21
	v_add_f32_e32 v2, v3, v2
	v_max_f32_e32 v10, 0, v2
	v_accvgpr_read_b32 v2, a22
	v_add_f32_e32 v2, v4, v2
	v_max_f32_e32 v11, 0, v2
	v_accvgpr_read_b32 v2, a23
	v_add_f32_e32 v2, v5, v2
	v_max_f32_e32 v12, 0, v2
	ds_read_b128 v[2:5], v22 offset:53824
	s_waitcnt lgkmcnt(0)
	v_add_f32_e32 v2, v13, v2
	v_max_f32_e32 v13, 0, v2
	v_accvgpr_read_b32 v2, a25
	v_add_f32_e32 v2, v3, v2
	v_max_f32_e32 v14, 0, v2
	v_accvgpr_read_b32 v2, a26
	v_add_f32_e32 v2, v4, v2
	v_max_f32_e32 v15, 0, v2
	v_accvgpr_read_b32 v2, a27
	v_add_f32_e32 v2, v5, v2
	v_max_f32_e32 v16, 0, v2
	ds_read_b128 v[2:5], v22 offset:53856
	s_waitcnt lgkmcnt(0)
	v_add_f32_e32 v2, v17, v2
	v_max_f32_e32 v17, 0, v2
	v_accvgpr_read_b32 v2, a29
	v_add_f32_e32 v2, v3, v2
	v_max_f32_e32 v18, 0, v2
	v_accvgpr_read_b32 v2, a30
	v_add_f32_e32 v2, v4, v2
	v_max_f32_e32 v19, 0, v2
	v_accvgpr_read_b32 v2, a31
	v_add_f32_e32 v2, v5, v2
	v_max_f32_e32 v20, 0, v2
	v_cvt_pk_f16_f32 v4, v9, v10
	v_cvt_pk_f16_f32 v3, v7, v8
	v_cvt_pk_f16_f32 v2, v1, v6
	ds_read_b128 v[6:9], v0 offset:49152
	v_cvt_pk_f16_f32 v5, v11, v12
	v_accvgpr_read_b32 v1, a0
	s_waitcnt lgkmcnt(0)
	v_mfma_f32_32x32x16_f16 a[32:47], v[6:9], v[2:5], a[32:47]
	ds_read_b128 v[6:9], v0 offset:50176
	v_cvt_pk_f16_f32 v5, v19, v20
	v_cvt_pk_f16_f32 v4, v17, v18
	v_cvt_pk_f16_f32 v3, v15, v16
	v_cvt_pk_f16_f32 v2, v13, v14
	v_accvgpr_read_b32 v13, a8
	v_accvgpr_read_b32 v17, a12
	s_waitcnt lgkmcnt(0)
	v_mfma_f32_32x32x16_f16 a[32:47], v[6:9], v[2:5], a[32:47]
	ds_read_b128 v[2:5], v22 offset:53888
	v_accvgpr_read_b32 v9, a4
	s_waitcnt lgkmcnt(0)
	v_add_f32_e32 v1, v1, v2
	v_accvgpr_read_b32 v2, a1
	v_add_f32_e32 v2, v3, v2
	v_max_f32_e32 v6, 0, v2
	v_accvgpr_read_b32 v2, a2
	v_add_f32_e32 v2, v4, v2
	v_max_f32_e32 v7, 0, v2
	v_accvgpr_read_b32 v2, a3
	v_add_f32_e32 v2, v5, v2
	v_max_f32_e32 v8, 0, v2
	ds_read_b128 v[2:5], v22 offset:53920
	v_max_f32_e32 v1, 0, v1
	s_waitcnt lgkmcnt(0)
	v_add_f32_e32 v2, v9, v2
	v_max_f32_e32 v9, 0, v2
	v_accvgpr_read_b32 v2, a5
	v_add_f32_e32 v2, v3, v2
	v_max_f32_e32 v10, 0, v2
	v_accvgpr_read_b32 v2, a6
	v_add_f32_e32 v2, v4, v2
	v_max_f32_e32 v11, 0, v2
	v_accvgpr_read_b32 v2, a7
	v_add_f32_e32 v2, v5, v2
	v_max_f32_e32 v12, 0, v2
	ds_read_b128 v[2:5], v22 offset:53952
	s_waitcnt lgkmcnt(0)
	v_add_f32_e32 v2, v13, v2
	v_max_f32_e32 v13, 0, v2
	v_accvgpr_read_b32 v2, a9
	v_add_f32_e32 v2, v3, v2
	v_max_f32_e32 v14, 0, v2
	v_accvgpr_read_b32 v2, a10
	v_add_f32_e32 v2, v4, v2
	v_max_f32_e32 v15, 0, v2
	v_accvgpr_read_b32 v2, a11
	v_add_f32_e32 v2, v5, v2
	v_max_f32_e32 v16, 0, v2
	ds_read_b128 v[2:5], v22 offset:53984
	s_waitcnt lgkmcnt(0)
	v_add_f32_e32 v2, v17, v2
	v_max_f32_e32 v17, 0, v2
	v_accvgpr_read_b32 v2, a13
	v_add_f32_e32 v2, v3, v2
	v_max_f32_e32 v18, 0, v2
	v_accvgpr_read_b32 v2, a14
	v_add_f32_e32 v2, v4, v2
	v_max_f32_e32 v19, 0, v2
	v_accvgpr_read_b32 v2, a15
	v_add_f32_e32 v2, v5, v2
	v_max_f32_e32 v20, 0, v2
	v_cvt_pk_f16_f32 v4, v9, v10
	v_cvt_pk_f16_f32 v3, v7, v8
	v_cvt_pk_f16_f32 v2, v1, v6
	ds_read_b128 v[6:9], v0 offset:51200
	v_cvt_pk_f16_f32 v5, v11, v12
	s_waitcnt lgkmcnt(0)
	s_nop 0
	v_mfma_f32_32x32x16_f16 a[32:47], v[6:9], v[2:5], a[32:47]
	ds_read_b128 v[6:9], v0 offset:52224
	v_cvt_pk_f16_f32 v5, v19, v20
	v_cvt_pk_f16_f32 v4, v17, v18
	v_cvt_pk_f16_f32 v3, v15, v16
	v_cvt_pk_f16_f32 v2, v13, v14
	s_waitcnt lgkmcnt(0)
	s_nop 0
	v_mfma_f32_32x32x16_f16 a[32:47], v[6:9], v[2:5], a[32:47]
	s_and_saveexec_b64 s[2:3], s[0:1]
	s_cbranch_execz .LBB3_39
	v_accvgpr_read_b32 v0, a80
	v_accvgpr_read_b32 v6, a86
	v_accvgpr_read_b32 v7, a87
	v_accvgpr_read_b32 v8, a88
	v_accvgpr_read_b32 v9, a89
	v_accvgpr_read_b32 v10, a90
	v_accvgpr_read_b32 v11, a91
	v_accvgpr_read_b32 v12, a92
	v_accvgpr_read_b32 v13, a93
	v_accvgpr_read_b32 v14, a94
	v_accvgpr_read_b32 v15, a95
	v_accvgpr_read_b32 v6, a32
	v_accvgpr_read_b32 v14, a40
	v_accvgpr_read_b32 v15, a41
	v_accvgpr_read_b32 v16, a42
	v_accvgpr_read_b32 v17, a43
	v_accvgpr_read_b32 v18, a44
	v_accvgpr_read_b32 v19, a45
	v_accvgpr_read_b32 v20, a46
	v_accvgpr_read_b32 v21, a47
	ds_read_b128 v[14:17], v22 offset:54016
	ds_read_b128 v[18:21], v22 offset:54080
	v_accvgpr_read_b32 v12, a38
	v_accvgpr_read_b32 v13, a39
	v_lshlrev_b32_e32 v24, 2, v85
	v_accvgpr_read_b32 v1, a81
	v_accvgpr_read_b32 v7, a33
	v_mad_i64_i32 v[12:13], s[0:1], v80, 40, s[18:19]
	v_ashrrev_i32_e32 v25, 31, v24
	v_accvgpr_read_b32 v3, a83
	v_accvgpr_read_b32 v9, a35
	v_lshl_add_u64 v[22:23], v[24:25], 2, v[12:13]
	v_mov_b32_e32 v25, v1
	s_waitcnt lgkmcnt(1)
	v_mov_b32_e32 v27, v15
	v_mov_b32_e32 v1, v7
	s_waitcnt lgkmcnt(0)
	v_mov_b32_e32 v15, v19
	v_accvgpr_read_b32 v2, a82
	v_accvgpr_read_b32 v8, a34
	v_pk_add_f32 v[0:1], v[0:1], v[14:15]
	v_mov_b32_e32 v7, v3
	v_mov_b32_e32 v15, v17
	v_mov_b32_e32 v3, v9
	v_mov_b32_e32 v17, v21
	v_mov_b32_e32 v24, v6
	v_mov_b32_e32 v26, v18
	v_mov_b32_e32 v6, v8
	v_mov_b32_e32 v14, v20
	v_pk_add_f32 v[2:3], v[2:3], v[16:17]
	v_pk_add_f32 v[24:25], v[24:25], v[26:27]
	s_waitcnt vmcnt(0)
	v_pk_mul_f32 v[0:1], v[82:83], v[0:1]
	v_pk_add_f32 v[6:7], v[6:7], v[14:15]
	v_pk_mul_f32 v[2:3], v[82:83], v[2:3]
	v_accvgpr_read_b32 v4, a84
	v_accvgpr_read_b32 v5, a85
	v_accvgpr_read_b32 v10, a36
	v_accvgpr_read_b32 v11, a37
	v_pk_fma_f32 v[0:1], v[82:83], v[24:25], v[0:1] op_sel:[1,0,0] op_sel_hi:[0,1,1]
	v_pk_fma_f32 v[2:3], v[82:83], v[6:7], v[2:3] op_sel:[1,0,0] op_sel_hi:[0,1,1]
	v_cmp_eq_u32_e32 vcc, 0, v85
	global_store_dwordx4 v[22:23], v[0:3], off
	s_and_b64 exec, exec, vcc
	s_cbranch_execz .LBB3_39
	s_mov_b32 s0, 0xd000
	v_add_u32_e64 v0, s0, 0
	ds_read2_b64 v[0:3], v0 offset0:100 offset1:108
	v_mov_b32_e32 v9, v5
	v_mov_b32_e32 v5, v11
	v_mov_b32_e32 v8, v10
	v_pk_mov_b32 v[6:7], v[82:83], v[82:83] op_sel:[1,0]
	s_waitcnt lgkmcnt(0)
	v_mov_b32_e32 v15, v1
	v_mov_b32_e32 v1, v3
	v_mov_b32_e32 v14, v2
	v_pk_add_f32 v[0:1], v[4:5], v[0:1]
	v_pk_add_f32 v[8:9], v[8:9], v[14:15]
	v_pk_mul_f32 v[0:1], v[82:83], v[0:1]
	s_nop 0
	v_pk_fma_f32 v[0:1], v[6:7], v[8:9], v[0:1]
	global_store_dwordx2 v[12:13], v[0:1], off offset:32
